# three quarters of the layer-1 w_down transposition moved out of the prologue: a quarter into the layer-0 idle slot, half into the layer-1 in-projection idle slot
# speedup vs baseline: 1.0034x; 1.0023x over previous
; #define GAS __attribute__((address_space(1)))
; #define LAS __attribute__((address_space(3)))
; #define LDS_WAIT() asm volatile("s_waitcnt lgkmcnt(0)" ::: "memory")
;     const int pr = item >> 1, kb = 2 * (pr / nblk) + (item & 1), nb = pr % nblk, k0 = 64 * kb, n0 = 32 * nb;
;     const int nr = n0 + (lane & 31); const int sc = MAP == 1 ? src_col_in(nr) : nr;
;     float v[32];
; #pragma unroll
;     for (int i = 0; i < 32; ++i) v[i] = sc >= 0 ? W[(size_t)(k0 + 2 * i + (lane >> 5)) * Nsrc + sc] : 0.f;
; #pragma unroll
;     for (int i = 0; i < 32; ++i) { const int k = k0 + 2 * i + (lane >> 5); float x = v[i] * wscale; if (KS) x *= (k < ksplit ? ksA[k] : ksB[k - ksplit]); scr[(2 * i + (lane >> 5)) * 33 + (lane & 31)] = x; }
;     LDS_WAIT(); asm volatile("" ::: "memory");
;     const int c = lane & 7;
; #pragma unroll
;     for (int j = 0; j < 4; ++j) { const int n = (lane >> 3) + 8 * j; const LAS float* s = scr + (8 * c) * 33 + n;
;         const unsigned long long o = (unsigned long long)pg8::pk4_fp8(s[0 * 33], s[1 * 33], s[2 * 33], s[3 * 33]) | ((unsigned long long)pg8::pk4_fp8(s[4 * 33], s[5 * 33], s[6 * 33], s[7 * 33]) << 32);
;         *(GAS unsigned long long*)(WT + (size_t)(n0 + n) * K + k0 + 8 * c) = o; }
;     LDS_WAIT(); asm volatile("" ::: "memory");
.LBB0_680:
	s_andn2_b64 vcc, exec, s[50:51]
	s_mov_b64 s[0:1], -1
	s_cbranch_vccnz .LBB0_579
	s_and_b64 vcc, exec, s[12:13]
	s_cbranch_vccz .Llite0_skip
	s_waitcnt vmcnt(0) lgkmcnt(0)
	s_barrier
	v_readlane_b32 s16, v253, 43
	s_sub_i32 s16, s16, 160
	v_and_b32_e32 v133, 63, v0
	v_lshrrev_b32_e32 v134, 6, v0
	v_lshrrev_b32_e32 v130, 5, v133
	v_lshl_add_u32 v131, v134, 4, v130
	v_and_b32_e32 v132, 31, v133
	v_xor_b32_e32 v132, v132, v134
	v_lshlrev_b32_e32 v132, 4, v132
	v_lshl_add_u32 v120, v131, 9, v132
	v_add_u32_e32 v121, 0x10000, v120
	v_and_b32_e32 v132, 31, v133
	v_lshlrev_b32_e32 v132, 4, v132
	s_mov_b32 s21, 0x4000
	v_mad_u32_u24 v126, v131, s21, v132
	v_and_b32_e32 v130, 7, v133
	v_lshrrev_b32_e32 v131, 5, v133
	v_lshl_add_u32 v131, v134, 2, v131
	v_xor_b32_e32 v131, v131, v130
	v_lshlrev_b32_e32 v131, 4, v131
	v_lshl_add_u32 v131, v130, 13, v131
	v_bfe_u32 v132, v133, 3, 2
	v_lshl_add_u32 v122, v132, 2, v131
	v_add_u32_e32 v123, 0x10000, v122
	v_and_b32_e32 v130, 7, v133
	v_lshrrev_b32_e32 v131, 5, v133
	v_lshl_add_u32 v131, v134, 2, v131
	v_add_u32_e32 v131, 2, v131
	v_xor_b32_e32 v131, v131, v130
	v_lshlrev_b32_e32 v131, 4, v131
	v_lshl_add_u32 v131, v130, 13, v131
	v_bfe_u32 v132, v133, 3, 2
	v_lshl_add_u32 v124, v132, 2, v131
	v_add_u32_e32 v125, 0x10000, v124
	v_lshrrev_b32_e32 v130, 3, v133
	v_lshl_add_u32 v130, v134, 4, v130
	v_and_b32_e32 v131, 7, v133
	v_lshlrev_b32_e32 v131, 4, v131
	v_lshl_add_u32 v127, v130, 14, v131
	v_lshrrev_b32_e32 v130, 3, v133
	v_lshl_add_u32 v130, v134, 4, v130
	v_add_u32_e32 v130, 8, v130
	v_and_b32_e32 v131, 7, v133
	v_lshlrev_b32_e32 v131, 4, v131
	v_lshl_add_u32 v128, v130, 14, v131
	v_mov_b32_e32 v129, 0x43e00000
	s_mov_b32 s20, 0xc3e00000
	v_readlane_b32 s2, v253, 35
	v_readlane_b32 s3, v253, 36
	v_readlane_b32 s4, v253, 41
	v_readlane_b32 s5, v253, 42
	s_add_u32 s2, s2, 0x10000000
	s_addc_u32 s3, s3, 0
	s_add_u32 s4, s4, 0x27600000
	s_addc_u32 s5, s5, 0
	s_add_i32 s17, s16, 0
	s_min_u32 s17, s17, 0x3ff
	s_lshr_b32 s18, s17, 5
	s_add_i32 s18, s18, 32
	s_and_b32 s19, s17, 31
	s_lshl_b32 s18, s18, 21
	s_lshl_b32 s19, s19, 9
	s_add_u32 s18, s18, s19
	s_add_u32 s10, s2, s18
	s_addc_u32 s11, s3, 0
	global_load_dwordx4 v[36:39], v126, s[10:11]
	s_add_u32 s10, s10, 0x8000
	s_addc_u32 s11, s11, 0
	global_load_dwordx4 v[40:43], v126, s[10:11]
	s_add_u32 s10, s10, 0x8000
	s_addc_u32 s11, s11, 0
	global_load_dwordx4 v[44:47], v126, s[10:11]
	s_add_u32 s10, s10, 0x8000
	s_addc_u32 s11, s11, 0
	global_load_dwordx4 v[48:51], v126, s[10:11]
	s_add_u32 s10, s10, 0x8000
	s_addc_u32 s11, s11, 0
	global_load_dwordx4 v[52:55], v126, s[10:11]
	s_add_u32 s10, s10, 0x8000
	s_addc_u32 s11, s11, 0
	global_load_dwordx4 v[56:59], v126, s[10:11]
	s_add_u32 s10, s10, 0x8000
	s_addc_u32 s11, s11, 0
	global_load_dwordx4 v[60:63], v126, s[10:11]
	s_add_u32 s10, s10, 0x8000
	s_addc_u32 s11, s11, 0
	global_load_dwordx4 v[64:67], v126, s[10:11]
	s_add_i32 s17, s16, 96
	s_min_u32 s17, s17, 0x3ff
	s_lshr_b32 s18, s17, 5
	s_add_i32 s18, s18, 32
	s_and_b32 s19, s17, 31
	s_lshl_b32 s18, s18, 21
	s_lshl_b32 s19, s19, 9
	s_add_u32 s18, s18, s19
	s_add_u32 s10, s2, s18
	s_addc_u32 s11, s3, 0
	global_load_dwordx4 v[68:71], v126, s[10:11]
	s_add_u32 s10, s10, 0x8000
	s_addc_u32 s11, s11, 0
	global_load_dwordx4 v[72:75], v126, s[10:11]
	s_add_u32 s10, s10, 0x8000
	s_addc_u32 s11, s11, 0
	global_load_dwordx4 v[76:79], v126, s[10:11]
	s_add_u32 s10, s10, 0x8000
	s_addc_u32 s11, s11, 0
	global_load_dwordx4 v[80:83], v126, s[10:11]
	s_add_u32 s10, s10, 0x8000
	s_addc_u32 s11, s11, 0
	global_load_dwordx4 v[84:87], v126, s[10:11]
	s_add_u32 s10, s10, 0x8000
	s_addc_u32 s11, s11, 0
	global_load_dwordx4 v[88:91], v126, s[10:11]
	s_add_u32 s10, s10, 0x8000
	s_addc_u32 s11, s11, 0
	global_load_dwordx4 v[92:95], v126, s[10:11]
	s_add_u32 s10, s10, 0x8000
	s_addc_u32 s11, s11, 0
	global_load_dwordx4 v[96:99], v126, s[10:11]
	s_waitcnt vmcnt(8)
	v_mul_f32_e32 v36, 0x43000000, v36
	v_mul_f32_e32 v37, 0x43000000, v37
	v_mul_f32_e32 v38, 0x43000000, v38
	v_mul_f32_e32 v39, 0x43000000, v39
	ds_write_b128 v120, v[36:39]
	v_mul_f32_e32 v40, 0x43000000, v40
	v_mul_f32_e32 v41, 0x43000000, v41
	v_mul_f32_e32 v42, 0x43000000, v42
	v_mul_f32_e32 v43, 0x43000000, v43
	ds_write_b128 v120, v[40:43] offset:1024
	v_mul_f32_e32 v44, 0x43000000, v44
	v_mul_f32_e32 v45, 0x43000000, v45
	v_mul_f32_e32 v46, 0x43000000, v46
	v_mul_f32_e32 v47, 0x43000000, v47
	ds_write_b128 v120, v[44:47] offset:2048
	v_mul_f32_e32 v48, 0x43000000, v48
	v_mul_f32_e32 v49, 0x43000000, v49
	v_mul_f32_e32 v50, 0x43000000, v50
	v_mul_f32_e32 v51, 0x43000000, v51
	ds_write_b128 v120, v[48:51] offset:3072
	v_mul_f32_e32 v52, 0x43000000, v52
	v_mul_f32_e32 v53, 0x43000000, v53
	v_mul_f32_e32 v54, 0x43000000, v54
	v_mul_f32_e32 v55, 0x43000000, v55
	ds_write_b128 v120, v[52:55] offset:4096
	v_mul_f32_e32 v56, 0x43000000, v56
	v_mul_f32_e32 v57, 0x43000000, v57
	v_mul_f32_e32 v58, 0x43000000, v58
	v_mul_f32_e32 v59, 0x43000000, v59
	ds_write_b128 v120, v[56:59] offset:5120
	v_mul_f32_e32 v60, 0x43000000, v60
	v_mul_f32_e32 v61, 0x43000000, v61
	v_mul_f32_e32 v62, 0x43000000, v62
	v_mul_f32_e32 v63, 0x43000000, v63
	ds_write_b128 v120, v[60:63] offset:6144
	v_mul_f32_e32 v64, 0x43000000, v64
	v_mul_f32_e32 v65, 0x43000000, v65
	v_mul_f32_e32 v66, 0x43000000, v66
	v_mul_f32_e32 v67, 0x43000000, v67
	ds_write_b128 v120, v[64:67] offset:7168
	s_waitcnt lgkmcnt(0)
	s_barrier
; #define GAS __attribute__((address_space(1)))
; #define LAS __attribute__((address_space(3)))
; #define LDS_WAIT() asm volatile("s_waitcnt lgkmcnt(0)" ::: "memory")
; __device__ __forceinline__ unsigned pk4_fp8(float a, float b, float c, float d) {
;     a = fminf(fmaxf(a, -448.f), 448.f); b = fminf(fmaxf(b, -448.f), 448.f); c = fminf(fmaxf(c, -448.f), 448.f); d = fminf(fmaxf(d, -448.f), 448.f);
;     int w = __builtin_amdgcn_cvt_pk_fp8_f32(a, b, 0, false); w = __builtin_amdgcn_cvt_pk_fp8_f32(c, d, w, true); return (unsigned)w; }
;     ...
;     for (int i = 0; i < 32; ++i) v[i] = sc >= 0 ? W[(size_t)(k0 + 2 * i + (lane >> 5)) * Nsrc + sc] : 0.f;
; #pragma unroll
;     for (int i = 0; i < 32; ++i) { const int k = k0 + 2 * i + (lane >> 5); float x = v[i] * wscale; if (KS) x *= (k < ksplit ? ksA[k] : ksB[k - ksplit]); scr[(2 * i + (lane >> 5)) * 33 + (lane & 31)] = x; }
;     LDS_WAIT(); asm volatile("" ::: "memory");
;     const int c = lane & 7;
; #pragma unroll
;     for (int j = 0; j < 4; ++j) { const int n = (lane >> 3) + 8 * j; const LAS float* s = scr + (8 * c) * 33 + n;
;         const unsigned long long o = (unsigned long long)pg8::pk4_fp8(s[0 * 33], s[1 * 33], s[2 * 33], s[3 * 33]) | ((unsigned long long)pg8::pk4_fp8(s[4 * 33], s[5 * 33], s[6 * 33], s[7 * 33]) << 32);
;         *(GAS unsigned long long*)(WT + (size_t)(n0 + n) * K + k0 + 8 * c) = o; }
	s_add_i32 s17, s16, 192
	s_min_u32 s17, s17, 0x3ff
	s_lshr_b32 s18, s17, 5
	s_add_i32 s18, s18, 32
	s_and_b32 s19, s17, 31
	s_lshl_b32 s18, s18, 21
	s_lshl_b32 s19, s19, 9
	s_add_u32 s18, s18, s19
	s_add_u32 s10, s2, s18
	s_addc_u32 s11, s3, 0
	global_load_dwordx4 v[36:39], v126, s[10:11]
	s_add_u32 s10, s10, 0x8000
	s_addc_u32 s11, s11, 0
	global_load_dwordx4 v[40:43], v126, s[10:11]
	s_add_u32 s10, s10, 0x8000
	s_addc_u32 s11, s11, 0
	global_load_dwordx4 v[44:47], v126, s[10:11]
	s_add_u32 s10, s10, 0x8000
	s_addc_u32 s11, s11, 0
	global_load_dwordx4 v[48:51], v126, s[10:11]
	s_add_u32 s10, s10, 0x8000
	s_addc_u32 s11, s11, 0
	global_load_dwordx4 v[52:55], v126, s[10:11]
	s_add_u32 s10, s10, 0x8000
	s_addc_u32 s11, s11, 0
	global_load_dwordx4 v[56:59], v126, s[10:11]
	s_add_u32 s10, s10, 0x8000
	s_addc_u32 s11, s11, 0
	global_load_dwordx4 v[60:63], v126, s[10:11]
	s_add_u32 s10, s10, 0x8000
	s_addc_u32 s11, s11, 0
	global_load_dwordx4 v[64:67], v126, s[10:11]
	s_add_i32 s17, s16, 0
	s_min_u32 s17, s17, 0x3ff
	s_lshr_b32 s18, s17, 5
	s_add_i32 s18, s18, 32
	s_and_b32 s19, s17, 31
	s_lshl_b32 s19, s19, 21
	s_lshl_b32 s18, s18, 7
	s_add_u32 s18, s18, s19
	s_add_u32 s14, s4, s18
	s_addc_u32 s15, s5, 0
	ds_read_b32 v100, v122
	ds_read_b32 v101, v122 offset:512
	ds_read_b32 v102, v122 offset:1024
	ds_read_b32 v103, v122 offset:1536
	ds_read_b32 v104, v122 offset:2048
	ds_read_b32 v105, v122 offset:2560
	ds_read_b32 v106, v122 offset:3072
	ds_read_b32 v107, v122 offset:3584
	ds_read_b32 v108, v122 offset:4096
	ds_read_b32 v109, v122 offset:4608
	ds_read_b32 v110, v122 offset:5120
	ds_read_b32 v111, v122 offset:5632
	ds_read_b32 v112, v122 offset:6144
	ds_read_b32 v113, v122 offset:6656
	ds_read_b32 v114, v122 offset:7168
	ds_read_b32 v115, v122 offset:7680
	s_waitcnt lgkmcnt(0)
	v_max_f32_e32 v100, v100, v100
	v_max_f32_e32 v101, v101, v101
	v_max_f32_e32 v102, v102, v102
	v_max_f32_e32 v103, v103, v103
	v_max_f32_e32 v104, v104, v104
	v_max_f32_e32 v105, v105, v105
	v_max_f32_e32 v106, v106, v106
	v_max_f32_e32 v107, v107, v107
	v_max_f32_e32 v108, v108, v108
	v_max_f32_e32 v109, v109, v109
	v_max_f32_e32 v110, v110, v110
	v_max_f32_e32 v111, v111, v111
	v_max_f32_e32 v112, v112, v112
	v_max_f32_e32 v113, v113, v113
	v_max_f32_e32 v114, v114, v114
	v_max_f32_e32 v115, v115, v115
	v_med3_f32 v100, v100, s20, v129
	v_med3_f32 v101, v101, s20, v129
	v_med3_f32 v102, v102, s20, v129
	v_med3_f32 v103, v103, s20, v129
	v_med3_f32 v104, v104, s20, v129
	v_med3_f32 v105, v105, s20, v129
	v_med3_f32 v106, v106, s20, v129
	v_med3_f32 v107, v107, s20, v129
	v_med3_f32 v108, v108, s20, v129
	v_med3_f32 v109, v109, s20, v129
	v_med3_f32 v110, v110, s20, v129
	v_med3_f32 v111, v111, s20, v129
	v_med3_f32 v112, v112, s20, v129
	v_med3_f32 v113, v113, s20, v129
	v_med3_f32 v114, v114, s20, v129
	v_med3_f32 v115, v115, s20, v129
	v_mov_b32_e32 v116, 0
	v_mov_b32_e32 v117, 0
	v_mov_b32_e32 v118, 0
	v_mov_b32_e32 v119, 0
	v_cvt_pk_fp8_f32 v116, v100, v101
	v_cvt_pk_fp8_f32 v117, v104, v105
	v_cvt_pk_fp8_f32 v118, v108, v109
	v_cvt_pk_fp8_f32 v119, v112, v113
	v_cvt_pk_fp8_f32 v116, v102, v103 op_sel:[0,0,1]
	v_cvt_pk_fp8_f32 v117, v106, v107 op_sel:[0,0,1]
	v_cvt_pk_fp8_f32 v118, v110, v111 op_sel:[0,0,1]
	v_cvt_pk_fp8_f32 v119, v114, v115 op_sel:[0,0,1]
	s_nop 0
	global_store_dwordx4 v127, v[116:119], s[14:15]
	ds_read_b32 v100, v124
	ds_read_b32 v101, v124 offset:512
	ds_read_b32 v102, v124 offset:1024
	ds_read_b32 v103, v124 offset:1536
	ds_read_b32 v104, v124 offset:2048
	ds_read_b32 v105, v124 offset:2560
	ds_read_b32 v106, v124 offset:3072
	ds_read_b32 v107, v124 offset:3584
	ds_read_b32 v108, v124 offset:4096
	ds_read_b32 v109, v124 offset:4608
	ds_read_b32 v110, v124 offset:5120
	ds_read_b32 v111, v124 offset:5632
	ds_read_b32 v112, v124 offset:6144
	ds_read_b32 v113, v124 offset:6656
	ds_read_b32 v114, v124 offset:7168
	ds_read_b32 v115, v124 offset:7680
	s_waitcnt lgkmcnt(0)
	v_max_f32_e32 v100, v100, v100
	v_max_f32_e32 v101, v101, v101
	v_max_f32_e32 v102, v102, v102
	v_max_f32_e32 v103, v103, v103
	v_max_f32_e32 v104, v104, v104
	v_max_f32_e32 v105, v105, v105
	v_max_f32_e32 v106, v106, v106
	v_max_f32_e32 v107, v107, v107
	v_max_f32_e32 v108, v108, v108
	v_max_f32_e32 v109, v109, v109
	v_max_f32_e32 v110, v110, v110
	v_max_f32_e32 v111, v111, v111
	v_max_f32_e32 v112, v112, v112
	v_max_f32_e32 v113, v113, v113
	v_max_f32_e32 v114, v114, v114
	v_max_f32_e32 v115, v115, v115
	v_med3_f32 v100, v100, s20, v129
	v_med3_f32 v101, v101, s20, v129
	v_med3_f32 v102, v102, s20, v129
	v_med3_f32 v103, v103, s20, v129
	v_med3_f32 v104, v104, s20, v129
	v_med3_f32 v105, v105, s20, v129
	v_med3_f32 v106, v106, s20, v129
	v_med3_f32 v107, v107, s20, v129
	v_med3_f32 v108, v108, s20, v129
	v_med3_f32 v109, v109, s20, v129
	v_med3_f32 v110, v110, s20, v129
	v_med3_f32 v111, v111, s20, v129
	v_med3_f32 v112, v112, s20, v129
	v_med3_f32 v113, v113, s20, v129
	v_med3_f32 v114, v114, s20, v129
	v_med3_f32 v115, v115, s20, v129
	v_mov_b32_e32 v116, 0
	v_mov_b32_e32 v117, 0
	v_mov_b32_e32 v118, 0
	v_mov_b32_e32 v119, 0
	v_cvt_pk_fp8_f32 v116, v100, v101
	v_cvt_pk_fp8_f32 v117, v104, v105
	v_cvt_pk_fp8_f32 v118, v108, v109
	v_cvt_pk_fp8_f32 v119, v112, v113
	v_cvt_pk_fp8_f32 v116, v102, v103 op_sel:[0,0,1]
	v_cvt_pk_fp8_f32 v117, v106, v107 op_sel:[0,0,1]
	v_cvt_pk_fp8_f32 v118, v110, v111 op_sel:[0,0,1]
	v_cvt_pk_fp8_f32 v119, v114, v115 op_sel:[0,0,1]
	s_nop 0
	global_store_dwordx4 v128, v[116:119], s[14:15]
	s_waitcnt vmcnt(10)
	v_mul_f32_e32 v68, 0x43000000, v68
	v_mul_f32_e32 v69, 0x43000000, v69
	v_mul_f32_e32 v70, 0x43000000, v70
	v_mul_f32_e32 v71, 0x43000000, v71
	ds_write_b128 v121, v[68:71]
	v_mul_f32_e32 v72, 0x43000000, v72
	v_mul_f32_e32 v73, 0x43000000, v73
	v_mul_f32_e32 v74, 0x43000000, v74
	v_mul_f32_e32 v75, 0x43000000, v75
	ds_write_b128 v121, v[72:75] offset:1024
	v_mul_f32_e32 v76, 0x43000000, v76
	v_mul_f32_e32 v77, 0x43000000, v77
	v_mul_f32_e32 v78, 0x43000000, v78
	v_mul_f32_e32 v79, 0x43000000, v79
	ds_write_b128 v121, v[76:79] offset:2048
	v_mul_f32_e32 v80, 0x43000000, v80
	v_mul_f32_e32 v81, 0x43000000, v81
	v_mul_f32_e32 v82, 0x43000000, v82
	v_mul_f32_e32 v83, 0x43000000, v83
	ds_write_b128 v121, v[80:83] offset:3072
	v_mul_f32_e32 v84, 0x43000000, v84
	v_mul_f32_e32 v85, 0x43000000, v85
	v_mul_f32_e32 v86, 0x43000000, v86
	v_mul_f32_e32 v87, 0x43000000, v87
	ds_write_b128 v121, v[84:87] offset:4096
	v_mul_f32_e32 v88, 0x43000000, v88
	v_mul_f32_e32 v89, 0x43000000, v89
	v_mul_f32_e32 v90, 0x43000000, v90
	v_mul_f32_e32 v91, 0x43000000, v91
	ds_write_b128 v121, v[88:91] offset:5120
	v_mul_f32_e32 v92, 0x43000000, v92
	v_mul_f32_e32 v93, 0x43000000, v93
	v_mul_f32_e32 v94, 0x43000000, v94
	v_mul_f32_e32 v95, 0x43000000, v95
	ds_write_b128 v121, v[92:95] offset:6144
	v_mul_f32_e32 v96, 0x43000000, v96
	v_mul_f32_e32 v97, 0x43000000, v97
	v_mul_f32_e32 v98, 0x43000000, v98
	v_mul_f32_e32 v99, 0x43000000, v99
	ds_write_b128 v121, v[96:99] offset:7168
	s_waitcnt lgkmcnt(0)
	s_barrier
; #define GAS __attribute__((address_space(1)))
; #define LAS __attribute__((address_space(3)))
; #define LDS_WAIT() asm volatile("s_waitcnt lgkmcnt(0)" ::: "memory")
; __device__ __forceinline__ unsigned pk4_fp8(float a, float b, float c, float d) {
;     a = fminf(fmaxf(a, -448.f), 448.f); b = fminf(fmaxf(b, -448.f), 448.f); c = fminf(fmaxf(c, -448.f), 448.f); d = fminf(fmaxf(d, -448.f), 448.f);
;     int w = __builtin_amdgcn_cvt_pk_fp8_f32(a, b, 0, false); w = __builtin_amdgcn_cvt_pk_fp8_f32(c, d, w, true); return (unsigned)w; }
;     ...
;     for (int i = 0; i < 32; ++i) v[i] = sc >= 0 ? W[(size_t)(k0 + 2 * i + (lane >> 5)) * Nsrc + sc] : 0.f;
; #pragma unroll
;     for (int i = 0; i < 32; ++i) { const int k = k0 + 2 * i + (lane >> 5); float x = v[i] * wscale; if (KS) x *= (k < ksplit ? ksA[k] : ksB[k - ksplit]); scr[(2 * i + (lane >> 5)) * 33 + (lane & 31)] = x; }
;     LDS_WAIT(); asm volatile("" ::: "memory");
;     const int c = lane & 7;
; #pragma unroll
;     for (int j = 0; j < 4; ++j) { const int n = (lane >> 3) + 8 * j; const LAS float* s = scr + (8 * c) * 33 + n;
;         const unsigned long long o = (unsigned long long)pg8::pk4_fp8(s[0 * 33], s[1 * 33], s[2 * 33], s[3 * 33]) | ((unsigned long long)pg8::pk4_fp8(s[4 * 33], s[5 * 33], s[6 * 33], s[7 * 33]) << 32);
;         *(GAS unsigned long long*)(WT + (size_t)(n0 + n) * K + k0 + 8 * c) = o; }
	s_add_i32 s17, s16, 288
	s_min_u32 s17, s17, 0x3ff
	s_lshr_b32 s18, s17, 5
	s_add_i32 s18, s18, 32
	s_and_b32 s19, s17, 31
	s_lshl_b32 s18, s18, 21
	s_lshl_b32 s19, s19, 9
	s_add_u32 s18, s18, s19
	s_add_u32 s10, s2, s18
	s_addc_u32 s11, s3, 0
	global_load_dwordx4 v[68:71], v126, s[10:11]
	s_add_u32 s10, s10, 0x8000
	s_addc_u32 s11, s11, 0
	global_load_dwordx4 v[72:75], v126, s[10:11]
	s_add_u32 s10, s10, 0x8000
	s_addc_u32 s11, s11, 0
	global_load_dwordx4 v[76:79], v126, s[10:11]
	s_add_u32 s10, s10, 0x8000
	s_addc_u32 s11, s11, 0
	global_load_dwordx4 v[80:83], v126, s[10:11]
	s_add_u32 s10, s10, 0x8000
	s_addc_u32 s11, s11, 0
	global_load_dwordx4 v[84:87], v126, s[10:11]
	s_add_u32 s10, s10, 0x8000
	s_addc_u32 s11, s11, 0
	global_load_dwordx4 v[88:91], v126, s[10:11]
	s_add_u32 s10, s10, 0x8000
	s_addc_u32 s11, s11, 0
	global_load_dwordx4 v[92:95], v126, s[10:11]
	s_add_u32 s10, s10, 0x8000
	s_addc_u32 s11, s11, 0
	global_load_dwordx4 v[96:99], v126, s[10:11]
	s_add_i32 s17, s16, 96
	s_min_u32 s17, s17, 0x3ff
	s_lshr_b32 s18, s17, 5
	s_add_i32 s18, s18, 32
	s_and_b32 s19, s17, 31
	s_lshl_b32 s19, s19, 21
	s_lshl_b32 s18, s18, 7
	s_add_u32 s18, s18, s19
	s_add_u32 s14, s4, s18
	s_addc_u32 s15, s5, 0
	ds_read_b32 v100, v123
	ds_read_b32 v101, v123 offset:512
	ds_read_b32 v102, v123 offset:1024
	ds_read_b32 v103, v123 offset:1536
	ds_read_b32 v104, v123 offset:2048
	ds_read_b32 v105, v123 offset:2560
	ds_read_b32 v106, v123 offset:3072
	ds_read_b32 v107, v123 offset:3584
	ds_read_b32 v108, v123 offset:4096
	ds_read_b32 v109, v123 offset:4608
	ds_read_b32 v110, v123 offset:5120
	ds_read_b32 v111, v123 offset:5632
	ds_read_b32 v112, v123 offset:6144
	ds_read_b32 v113, v123 offset:6656
	ds_read_b32 v114, v123 offset:7168
	ds_read_b32 v115, v123 offset:7680
	s_waitcnt lgkmcnt(0)
	v_max_f32_e32 v100, v100, v100
	v_max_f32_e32 v101, v101, v101
	v_max_f32_e32 v102, v102, v102
	v_max_f32_e32 v103, v103, v103
	v_max_f32_e32 v104, v104, v104
	v_max_f32_e32 v105, v105, v105
	v_max_f32_e32 v106, v106, v106
	v_max_f32_e32 v107, v107, v107
	v_max_f32_e32 v108, v108, v108
	v_max_f32_e32 v109, v109, v109
	v_max_f32_e32 v110, v110, v110
	v_max_f32_e32 v111, v111, v111
	v_max_f32_e32 v112, v112, v112
	v_max_f32_e32 v113, v113, v113
	v_max_f32_e32 v114, v114, v114
	v_max_f32_e32 v115, v115, v115
	v_med3_f32 v100, v100, s20, v129
	v_med3_f32 v101, v101, s20, v129
	v_med3_f32 v102, v102, s20, v129
	v_med3_f32 v103, v103, s20, v129
	v_med3_f32 v104, v104, s20, v129
	v_med3_f32 v105, v105, s20, v129
	v_med3_f32 v106, v106, s20, v129
	v_med3_f32 v107, v107, s20, v129
	v_med3_f32 v108, v108, s20, v129
	v_med3_f32 v109, v109, s20, v129
	v_med3_f32 v110, v110, s20, v129
	v_med3_f32 v111, v111, s20, v129
	v_med3_f32 v112, v112, s20, v129
	v_med3_f32 v113, v113, s20, v129
	v_med3_f32 v114, v114, s20, v129
	v_med3_f32 v115, v115, s20, v129
	v_mov_b32_e32 v116, 0
	v_mov_b32_e32 v117, 0
	v_mov_b32_e32 v118, 0
	v_mov_b32_e32 v119, 0
	v_cvt_pk_fp8_f32 v116, v100, v101
	v_cvt_pk_fp8_f32 v117, v104, v105
	v_cvt_pk_fp8_f32 v118, v108, v109
	v_cvt_pk_fp8_f32 v119, v112, v113
	v_cvt_pk_fp8_f32 v116, v102, v103 op_sel:[0,0,1]
	v_cvt_pk_fp8_f32 v117, v106, v107 op_sel:[0,0,1]
	v_cvt_pk_fp8_f32 v118, v110, v111 op_sel:[0,0,1]
	v_cvt_pk_fp8_f32 v119, v114, v115 op_sel:[0,0,1]
	s_nop 0
	global_store_dwordx4 v127, v[116:119], s[14:15]
	ds_read_b32 v100, v125
	ds_read_b32 v101, v125 offset:512
	ds_read_b32 v102, v125 offset:1024
	ds_read_b32 v103, v125 offset:1536
	ds_read_b32 v104, v125 offset:2048
	ds_read_b32 v105, v125 offset:2560
	ds_read_b32 v106, v125 offset:3072
	ds_read_b32 v107, v125 offset:3584
	ds_read_b32 v108, v125 offset:4096
	ds_read_b32 v109, v125 offset:4608
	ds_read_b32 v110, v125 offset:5120
	ds_read_b32 v111, v125 offset:5632
	ds_read_b32 v112, v125 offset:6144
	ds_read_b32 v113, v125 offset:6656
	ds_read_b32 v114, v125 offset:7168
	ds_read_b32 v115, v125 offset:7680
	s_waitcnt lgkmcnt(0)
	v_max_f32_e32 v100, v100, v100
	v_max_f32_e32 v101, v101, v101
	v_max_f32_e32 v102, v102, v102
	v_max_f32_e32 v103, v103, v103
	v_max_f32_e32 v104, v104, v104
	v_max_f32_e32 v105, v105, v105
	v_max_f32_e32 v106, v106, v106
	v_max_f32_e32 v107, v107, v107
	v_max_f32_e32 v108, v108, v108
	v_max_f32_e32 v109, v109, v109
	v_max_f32_e32 v110, v110, v110
	v_max_f32_e32 v111, v111, v111
	v_max_f32_e32 v112, v112, v112
	v_max_f32_e32 v113, v113, v113
	v_max_f32_e32 v114, v114, v114
	v_max_f32_e32 v115, v115, v115
	v_med3_f32 v100, v100, s20, v129
	v_med3_f32 v101, v101, s20, v129
	v_med3_f32 v102, v102, s20, v129
	v_med3_f32 v103, v103, s20, v129
	v_med3_f32 v104, v104, s20, v129
	v_med3_f32 v105, v105, s20, v129
	v_med3_f32 v106, v106, s20, v129
	v_med3_f32 v107, v107, s20, v129
	v_med3_f32 v108, v108, s20, v129
	v_med3_f32 v109, v109, s20, v129
	v_med3_f32 v110, v110, s20, v129
	v_med3_f32 v111, v111, s20, v129
	v_med3_f32 v112, v112, s20, v129
	v_med3_f32 v113, v113, s20, v129
	v_med3_f32 v114, v114, s20, v129
	v_med3_f32 v115, v115, s20, v129
	v_mov_b32_e32 v116, 0
	v_mov_b32_e32 v117, 0
	v_mov_b32_e32 v118, 0
	v_mov_b32_e32 v119, 0
	v_cvt_pk_fp8_f32 v116, v100, v101
	v_cvt_pk_fp8_f32 v117, v104, v105
	v_cvt_pk_fp8_f32 v118, v108, v109
	v_cvt_pk_fp8_f32 v119, v112, v113
	v_cvt_pk_fp8_f32 v116, v102, v103 op_sel:[0,0,1]
	v_cvt_pk_fp8_f32 v117, v106, v107 op_sel:[0,0,1]
	v_cvt_pk_fp8_f32 v118, v110, v111 op_sel:[0,0,1]
	v_cvt_pk_fp8_f32 v119, v114, v115 op_sel:[0,0,1]
	s_nop 0
	global_store_dwordx4 v128, v[116:119], s[14:15]
	s_waitcnt vmcnt(12)
	v_mul_f32_e32 v36, 0x43000000, v36
	v_mul_f32_e32 v37, 0x43000000, v37
	v_mul_f32_e32 v38, 0x43000000, v38
	v_mul_f32_e32 v39, 0x43000000, v39
	ds_write_b128 v120, v[36:39]
	v_mul_f32_e32 v40, 0x43000000, v40
	v_mul_f32_e32 v41, 0x43000000, v41
	v_mul_f32_e32 v42, 0x43000000, v42
	v_mul_f32_e32 v43, 0x43000000, v43
	ds_write_b128 v120, v[40:43] offset:1024
	v_mul_f32_e32 v44, 0x43000000, v44
	v_mul_f32_e32 v45, 0x43000000, v45
	v_mul_f32_e32 v46, 0x43000000, v46
	v_mul_f32_e32 v47, 0x43000000, v47
	ds_write_b128 v120, v[44:47] offset:2048
	v_mul_f32_e32 v48, 0x43000000, v48
	v_mul_f32_e32 v49, 0x43000000, v49
	v_mul_f32_e32 v50, 0x43000000, v50
	v_mul_f32_e32 v51, 0x43000000, v51
	ds_write_b128 v120, v[48:51] offset:3072
	v_mul_f32_e32 v52, 0x43000000, v52
	v_mul_f32_e32 v53, 0x43000000, v53
	v_mul_f32_e32 v54, 0x43000000, v54
	v_mul_f32_e32 v55, 0x43000000, v55
	ds_write_b128 v120, v[52:55] offset:4096
	v_mul_f32_e32 v56, 0x43000000, v56
	v_mul_f32_e32 v57, 0x43000000, v57
	v_mul_f32_e32 v58, 0x43000000, v58
	v_mul_f32_e32 v59, 0x43000000, v59
	ds_write_b128 v120, v[56:59] offset:5120
	v_mul_f32_e32 v60, 0x43000000, v60
	v_mul_f32_e32 v61, 0x43000000, v61
	v_mul_f32_e32 v62, 0x43000000, v62
	v_mul_f32_e32 v63, 0x43000000, v63
	ds_write_b128 v120, v[60:63] offset:6144
	v_mul_f32_e32 v64, 0x43000000, v64
	v_mul_f32_e32 v65, 0x43000000, v65
	v_mul_f32_e32 v66, 0x43000000, v66
	v_mul_f32_e32 v67, 0x43000000, v67
	ds_write_b128 v120, v[64:67] offset:7168
	s_waitcnt lgkmcnt(0)
	s_barrier
; #define GAS __attribute__((address_space(1)))
; #define LAS __attribute__((address_space(3)))
; #define LDS_WAIT() asm volatile("s_waitcnt lgkmcnt(0)" ::: "memory")
; __device__ __forceinline__ unsigned pk4_fp8(float a, float b, float c, float d) {
;     a = fminf(fmaxf(a, -448.f), 448.f); b = fminf(fmaxf(b, -448.f), 448.f); c = fminf(fmaxf(c, -448.f), 448.f); d = fminf(fmaxf(d, -448.f), 448.f);
;     int w = __builtin_amdgcn_cvt_pk_fp8_f32(a, b, 0, false); w = __builtin_amdgcn_cvt_pk_fp8_f32(c, d, w, true); return (unsigned)w; }
;     ...
;     for (int i = 0; i < 32; ++i) v[i] = sc >= 0 ? W[(size_t)(k0 + 2 * i + (lane >> 5)) * Nsrc + sc] : 0.f;
; #pragma unroll
;     for (int i = 0; i < 32; ++i) { const int k = k0 + 2 * i + (lane >> 5); float x = v[i] * wscale; if (KS) x *= (k < ksplit ? ksA[k] : ksB[k - ksplit]); scr[(2 * i + (lane >> 5)) * 33 + (lane & 31)] = x; }
;     LDS_WAIT(); asm volatile("" ::: "memory");
;     const int c = lane & 7;
; #pragma unroll
;     for (int j = 0; j < 4; ++j) { const int n = (lane >> 3) + 8 * j; const LAS float* s = scr + (8 * c) * 33 + n;
;         const unsigned long long o = (unsigned long long)pg8::pk4_fp8(s[0 * 33], s[1 * 33], s[2 * 33], s[3 * 33]) | ((unsigned long long)pg8::pk4_fp8(s[4 * 33], s[5 * 33], s[6 * 33], s[7 * 33]) << 32);
;         *(GAS unsigned long long*)(WT + (size_t)(n0 + n) * K + k0 + 8 * c) = o; }
	s_add_i32 s17, s16, 384
	s_min_u32 s17, s17, 0x3ff
	s_lshr_b32 s18, s17, 5
	s_add_i32 s18, s18, 32
	s_and_b32 s19, s17, 31
	s_lshl_b32 s18, s18, 21
	s_lshl_b32 s19, s19, 9
	s_add_u32 s18, s18, s19
	s_add_u32 s10, s2, s18
	s_addc_u32 s11, s3, 0
	global_load_dwordx4 v[36:39], v126, s[10:11]
	s_add_u32 s10, s10, 0x8000
	s_addc_u32 s11, s11, 0
	global_load_dwordx4 v[40:43], v126, s[10:11]
	s_add_u32 s10, s10, 0x8000
	s_addc_u32 s11, s11, 0
	global_load_dwordx4 v[44:47], v126, s[10:11]
	s_add_u32 s10, s10, 0x8000
	s_addc_u32 s11, s11, 0
	global_load_dwordx4 v[48:51], v126, s[10:11]
	s_add_u32 s10, s10, 0x8000
	s_addc_u32 s11, s11, 0
	global_load_dwordx4 v[52:55], v126, s[10:11]
	s_add_u32 s10, s10, 0x8000
	s_addc_u32 s11, s11, 0
	global_load_dwordx4 v[56:59], v126, s[10:11]
	s_add_u32 s10, s10, 0x8000
	s_addc_u32 s11, s11, 0
	global_load_dwordx4 v[60:63], v126, s[10:11]
	s_add_u32 s10, s10, 0x8000
	s_addc_u32 s11, s11, 0
	global_load_dwordx4 v[64:67], v126, s[10:11]
	s_add_i32 s17, s16, 192
	s_min_u32 s17, s17, 0x3ff
	s_lshr_b32 s18, s17, 5
	s_add_i32 s18, s18, 32
	s_and_b32 s19, s17, 31
	s_lshl_b32 s19, s19, 21
	s_lshl_b32 s18, s18, 7
	s_add_u32 s18, s18, s19
	s_add_u32 s14, s4, s18
	s_addc_u32 s15, s5, 0
	ds_read_b32 v100, v122
	ds_read_b32 v101, v122 offset:512
	ds_read_b32 v102, v122 offset:1024
	ds_read_b32 v103, v122 offset:1536
	ds_read_b32 v104, v122 offset:2048
	ds_read_b32 v105, v122 offset:2560
	ds_read_b32 v106, v122 offset:3072
	ds_read_b32 v107, v122 offset:3584
	ds_read_b32 v108, v122 offset:4096
	ds_read_b32 v109, v122 offset:4608
	ds_read_b32 v110, v122 offset:5120
	ds_read_b32 v111, v122 offset:5632
	ds_read_b32 v112, v122 offset:6144
	ds_read_b32 v113, v122 offset:6656
	ds_read_b32 v114, v122 offset:7168
	ds_read_b32 v115, v122 offset:7680
	s_waitcnt lgkmcnt(0)
	v_max_f32_e32 v100, v100, v100
	v_max_f32_e32 v101, v101, v101
	v_max_f32_e32 v102, v102, v102
	v_max_f32_e32 v103, v103, v103
	v_max_f32_e32 v104, v104, v104
	v_max_f32_e32 v105, v105, v105
	v_max_f32_e32 v106, v106, v106
	v_max_f32_e32 v107, v107, v107
	v_max_f32_e32 v108, v108, v108
	v_max_f32_e32 v109, v109, v109
	v_max_f32_e32 v110, v110, v110
	v_max_f32_e32 v111, v111, v111
	v_max_f32_e32 v112, v112, v112
	v_max_f32_e32 v113, v113, v113
	v_max_f32_e32 v114, v114, v114
	v_max_f32_e32 v115, v115, v115
	v_med3_f32 v100, v100, s20, v129
	v_med3_f32 v101, v101, s20, v129
	v_med3_f32 v102, v102, s20, v129
	v_med3_f32 v103, v103, s20, v129
	v_med3_f32 v104, v104, s20, v129
	v_med3_f32 v105, v105, s20, v129
	v_med3_f32 v106, v106, s20, v129
	v_med3_f32 v107, v107, s20, v129
	v_med3_f32 v108, v108, s20, v129
	v_med3_f32 v109, v109, s20, v129
	v_med3_f32 v110, v110, s20, v129
	v_med3_f32 v111, v111, s20, v129
	v_med3_f32 v112, v112, s20, v129
	v_med3_f32 v113, v113, s20, v129
	v_med3_f32 v114, v114, s20, v129
	v_med3_f32 v115, v115, s20, v129
	v_mov_b32_e32 v116, 0
	v_mov_b32_e32 v117, 0
	v_mov_b32_e32 v118, 0
	v_mov_b32_e32 v119, 0
	v_cvt_pk_fp8_f32 v116, v100, v101
	v_cvt_pk_fp8_f32 v117, v104, v105
	v_cvt_pk_fp8_f32 v118, v108, v109
	v_cvt_pk_fp8_f32 v119, v112, v113
	v_cvt_pk_fp8_f32 v116, v102, v103 op_sel:[0,0,1]
	v_cvt_pk_fp8_f32 v117, v106, v107 op_sel:[0,0,1]
	v_cvt_pk_fp8_f32 v118, v110, v111 op_sel:[0,0,1]
	v_cvt_pk_fp8_f32 v119, v114, v115 op_sel:[0,0,1]
	s_nop 0
	global_store_dwordx4 v127, v[116:119], s[14:15]
	ds_read_b32 v100, v124
	ds_read_b32 v101, v124 offset:512
	ds_read_b32 v102, v124 offset:1024
	ds_read_b32 v103, v124 offset:1536
	ds_read_b32 v104, v124 offset:2048
	ds_read_b32 v105, v124 offset:2560
	ds_read_b32 v106, v124 offset:3072
	ds_read_b32 v107, v124 offset:3584
	ds_read_b32 v108, v124 offset:4096
	ds_read_b32 v109, v124 offset:4608
	ds_read_b32 v110, v124 offset:5120
	ds_read_b32 v111, v124 offset:5632
	ds_read_b32 v112, v124 offset:6144
	ds_read_b32 v113, v124 offset:6656
	ds_read_b32 v114, v124 offset:7168
	ds_read_b32 v115, v124 offset:7680
	s_waitcnt lgkmcnt(0)
	v_max_f32_e32 v100, v100, v100
	v_max_f32_e32 v101, v101, v101
	v_max_f32_e32 v102, v102, v102
	v_max_f32_e32 v103, v103, v103
	v_max_f32_e32 v104, v104, v104
	v_max_f32_e32 v105, v105, v105
	v_max_f32_e32 v106, v106, v106
	v_max_f32_e32 v107, v107, v107
	v_max_f32_e32 v108, v108, v108
	v_max_f32_e32 v109, v109, v109
	v_max_f32_e32 v110, v110, v110
	v_max_f32_e32 v111, v111, v111
	v_max_f32_e32 v112, v112, v112
	v_max_f32_e32 v113, v113, v113
	v_max_f32_e32 v114, v114, v114
	v_max_f32_e32 v115, v115, v115
	v_med3_f32 v100, v100, s20, v129
	v_med3_f32 v101, v101, s20, v129
	v_med3_f32 v102, v102, s20, v129
	v_med3_f32 v103, v103, s20, v129
	v_med3_f32 v104, v104, s20, v129
	v_med3_f32 v105, v105, s20, v129
	v_med3_f32 v106, v106, s20, v129
	v_med3_f32 v107, v107, s20, v129
	v_med3_f32 v108, v108, s20, v129
	v_med3_f32 v109, v109, s20, v129
	v_med3_f32 v110, v110, s20, v129
	v_med3_f32 v111, v111, s20, v129
	v_med3_f32 v112, v112, s20, v129
	v_med3_f32 v113, v113, s20, v129
	v_med3_f32 v114, v114, s20, v129
	v_med3_f32 v115, v115, s20, v129
	v_mov_b32_e32 v116, 0
	v_mov_b32_e32 v117, 0
	v_mov_b32_e32 v118, 0
	v_mov_b32_e32 v119, 0
	v_cvt_pk_fp8_f32 v116, v100, v101
	v_cvt_pk_fp8_f32 v117, v104, v105
	v_cvt_pk_fp8_f32 v118, v108, v109
	v_cvt_pk_fp8_f32 v119, v112, v113
	v_cvt_pk_fp8_f32 v116, v102, v103 op_sel:[0,0,1]
	v_cvt_pk_fp8_f32 v117, v106, v107 op_sel:[0,0,1]
	v_cvt_pk_fp8_f32 v118, v110, v111 op_sel:[0,0,1]
	v_cvt_pk_fp8_f32 v119, v114, v115 op_sel:[0,0,1]
	s_nop 0
	global_store_dwordx4 v128, v[116:119], s[14:15]
	s_waitcnt vmcnt(12)
	v_mul_f32_e32 v68, 0x43000000, v68
	v_mul_f32_e32 v69, 0x43000000, v69
	v_mul_f32_e32 v70, 0x43000000, v70
	v_mul_f32_e32 v71, 0x43000000, v71
	ds_write_b128 v121, v[68:71]
	v_mul_f32_e32 v72, 0x43000000, v72
	v_mul_f32_e32 v73, 0x43000000, v73
	v_mul_f32_e32 v74, 0x43000000, v74
	v_mul_f32_e32 v75, 0x43000000, v75
	ds_write_b128 v121, v[72:75] offset:1024
	v_mul_f32_e32 v76, 0x43000000, v76
	v_mul_f32_e32 v77, 0x43000000, v77
	v_mul_f32_e32 v78, 0x43000000, v78
	v_mul_f32_e32 v79, 0x43000000, v79
	ds_write_b128 v121, v[76:79] offset:2048
	v_mul_f32_e32 v80, 0x43000000, v80
	v_mul_f32_e32 v81, 0x43000000, v81
	v_mul_f32_e32 v82, 0x43000000, v82
	v_mul_f32_e32 v83, 0x43000000, v83
	ds_write_b128 v121, v[80:83] offset:3072
	v_mul_f32_e32 v84, 0x43000000, v84
	v_mul_f32_e32 v85, 0x43000000, v85
	v_mul_f32_e32 v86, 0x43000000, v86
	v_mul_f32_e32 v87, 0x43000000, v87
	ds_write_b128 v121, v[84:87] offset:4096
	v_mul_f32_e32 v88, 0x43000000, v88
	v_mul_f32_e32 v89, 0x43000000, v89
	v_mul_f32_e32 v90, 0x43000000, v90
	v_mul_f32_e32 v91, 0x43000000, v91
	ds_write_b128 v121, v[88:91] offset:5120
	v_mul_f32_e32 v92, 0x43000000, v92
	v_mul_f32_e32 v93, 0x43000000, v93
	v_mul_f32_e32 v94, 0x43000000, v94
	v_mul_f32_e32 v95, 0x43000000, v95
	ds_write_b128 v121, v[92:95] offset:6144
	v_mul_f32_e32 v96, 0x43000000, v96
	v_mul_f32_e32 v97, 0x43000000, v97
	v_mul_f32_e32 v98, 0x43000000, v98
	v_mul_f32_e32 v99, 0x43000000, v99
	ds_write_b128 v121, v[96:99] offset:7168
	s_waitcnt lgkmcnt(0)
	s_barrier
; #define GAS __attribute__((address_space(1)))
; #define LAS __attribute__((address_space(3)))
; #define LDS_WAIT() asm volatile("s_waitcnt lgkmcnt(0)" ::: "memory")
; __device__ __forceinline__ unsigned pk4_fp8(float a, float b, float c, float d) {
;     a = fminf(fmaxf(a, -448.f), 448.f); b = fminf(fmaxf(b, -448.f), 448.f); c = fminf(fmaxf(c, -448.f), 448.f); d = fminf(fmaxf(d, -448.f), 448.f);
;     int w = __builtin_amdgcn_cvt_pk_fp8_f32(a, b, 0, false); w = __builtin_amdgcn_cvt_pk_fp8_f32(c, d, w, true); return (unsigned)w; }
;     ...
;     for (int i = 0; i < 32; ++i) v[i] = sc >= 0 ? W[(size_t)(k0 + 2 * i + (lane >> 5)) * Nsrc + sc] : 0.f;
; #pragma unroll
;     for (int i = 0; i < 32; ++i) { const int k = k0 + 2 * i + (lane >> 5); float x = v[i] * wscale; if (KS) x *= (k < ksplit ? ksA[k] : ksB[k - ksplit]); scr[(2 * i + (lane >> 5)) * 33 + (lane & 31)] = x; }
;     LDS_WAIT(); asm volatile("" ::: "memory");
;     const int c = lane & 7;
; #pragma unroll
;     for (int j = 0; j < 4; ++j) { const int n = (lane >> 3) + 8 * j; const LAS float* s = scr + (8 * c) * 33 + n;
;         const unsigned long long o = (unsigned long long)pg8::pk4_fp8(s[0 * 33], s[1 * 33], s[2 * 33], s[3 * 33]) | ((unsigned long long)pg8::pk4_fp8(s[4 * 33], s[5 * 33], s[6 * 33], s[7 * 33]) << 32);
;         *(GAS unsigned long long*)(WT + (size_t)(n0 + n) * K + k0 + 8 * c) = o; }
	s_add_i32 s17, s16, 480
	s_min_u32 s17, s17, 0x3ff
	s_lshr_b32 s18, s17, 5
	s_add_i32 s18, s18, 32
	s_and_b32 s19, s17, 31
	s_lshl_b32 s18, s18, 21
	s_lshl_b32 s19, s19, 9
	s_add_u32 s18, s18, s19
	s_add_u32 s10, s2, s18
	s_addc_u32 s11, s3, 0
	global_load_dwordx4 v[68:71], v126, s[10:11]
	s_add_u32 s10, s10, 0x8000
	s_addc_u32 s11, s11, 0
	global_load_dwordx4 v[72:75], v126, s[10:11]
	s_add_u32 s10, s10, 0x8000
	s_addc_u32 s11, s11, 0
	global_load_dwordx4 v[76:79], v126, s[10:11]
	s_add_u32 s10, s10, 0x8000
	s_addc_u32 s11, s11, 0
	global_load_dwordx4 v[80:83], v126, s[10:11]
	s_add_u32 s10, s10, 0x8000
	s_addc_u32 s11, s11, 0
	global_load_dwordx4 v[84:87], v126, s[10:11]
	s_add_u32 s10, s10, 0x8000
	s_addc_u32 s11, s11, 0
	global_load_dwordx4 v[88:91], v126, s[10:11]
	s_add_u32 s10, s10, 0x8000
	s_addc_u32 s11, s11, 0
	global_load_dwordx4 v[92:95], v126, s[10:11]
	s_add_u32 s10, s10, 0x8000
	s_addc_u32 s11, s11, 0
	global_load_dwordx4 v[96:99], v126, s[10:11]
	s_add_i32 s17, s16, 288
	s_min_u32 s17, s17, 0x3ff
	s_lshr_b32 s18, s17, 5
	s_add_i32 s18, s18, 32
	s_and_b32 s19, s17, 31
	s_lshl_b32 s19, s19, 21
	s_lshl_b32 s18, s18, 7
	s_add_u32 s18, s18, s19
	s_add_u32 s14, s4, s18
	s_addc_u32 s15, s5, 0
	ds_read_b32 v100, v123
	ds_read_b32 v101, v123 offset:512
	ds_read_b32 v102, v123 offset:1024
	ds_read_b32 v103, v123 offset:1536
	ds_read_b32 v104, v123 offset:2048
	ds_read_b32 v105, v123 offset:2560
	ds_read_b32 v106, v123 offset:3072
	ds_read_b32 v107, v123 offset:3584
	ds_read_b32 v108, v123 offset:4096
	ds_read_b32 v109, v123 offset:4608
	ds_read_b32 v110, v123 offset:5120
	ds_read_b32 v111, v123 offset:5632
	ds_read_b32 v112, v123 offset:6144
	ds_read_b32 v113, v123 offset:6656
	ds_read_b32 v114, v123 offset:7168
	ds_read_b32 v115, v123 offset:7680
	s_waitcnt lgkmcnt(0)
	v_max_f32_e32 v100, v100, v100
	v_max_f32_e32 v101, v101, v101
	v_max_f32_e32 v102, v102, v102
	v_max_f32_e32 v103, v103, v103
	v_max_f32_e32 v104, v104, v104
	v_max_f32_e32 v105, v105, v105
	v_max_f32_e32 v106, v106, v106
	v_max_f32_e32 v107, v107, v107
	v_max_f32_e32 v108, v108, v108
	v_max_f32_e32 v109, v109, v109
	v_max_f32_e32 v110, v110, v110
	v_max_f32_e32 v111, v111, v111
	v_max_f32_e32 v112, v112, v112
	v_max_f32_e32 v113, v113, v113
	v_max_f32_e32 v114, v114, v114
	v_max_f32_e32 v115, v115, v115
	v_med3_f32 v100, v100, s20, v129
	v_med3_f32 v101, v101, s20, v129
	v_med3_f32 v102, v102, s20, v129
	v_med3_f32 v103, v103, s20, v129
	v_med3_f32 v104, v104, s20, v129
	v_med3_f32 v105, v105, s20, v129
	v_med3_f32 v106, v106, s20, v129
	v_med3_f32 v107, v107, s20, v129
	v_med3_f32 v108, v108, s20, v129
	v_med3_f32 v109, v109, s20, v129
	v_med3_f32 v110, v110, s20, v129
	v_med3_f32 v111, v111, s20, v129
	v_med3_f32 v112, v112, s20, v129
	v_med3_f32 v113, v113, s20, v129
	v_med3_f32 v114, v114, s20, v129
	v_med3_f32 v115, v115, s20, v129
	v_mov_b32_e32 v116, 0
	v_mov_b32_e32 v117, 0
	v_mov_b32_e32 v118, 0
	v_mov_b32_e32 v119, 0
	v_cvt_pk_fp8_f32 v116, v100, v101
	v_cvt_pk_fp8_f32 v117, v104, v105
	v_cvt_pk_fp8_f32 v118, v108, v109
	v_cvt_pk_fp8_f32 v119, v112, v113
	v_cvt_pk_fp8_f32 v116, v102, v103 op_sel:[0,0,1]
	v_cvt_pk_fp8_f32 v117, v106, v107 op_sel:[0,0,1]
	v_cvt_pk_fp8_f32 v118, v110, v111 op_sel:[0,0,1]
	v_cvt_pk_fp8_f32 v119, v114, v115 op_sel:[0,0,1]
	s_nop 0
	global_store_dwordx4 v127, v[116:119], s[14:15]
	ds_read_b32 v100, v125
	ds_read_b32 v101, v125 offset:512
	ds_read_b32 v102, v125 offset:1024
	ds_read_b32 v103, v125 offset:1536
	ds_read_b32 v104, v125 offset:2048
	ds_read_b32 v105, v125 offset:2560
	ds_read_b32 v106, v125 offset:3072
	ds_read_b32 v107, v125 offset:3584
	ds_read_b32 v108, v125 offset:4096
	ds_read_b32 v109, v125 offset:4608
	ds_read_b32 v110, v125 offset:5120
	ds_read_b32 v111, v125 offset:5632
	ds_read_b32 v112, v125 offset:6144
	ds_read_b32 v113, v125 offset:6656
	ds_read_b32 v114, v125 offset:7168
	ds_read_b32 v115, v125 offset:7680
	s_waitcnt lgkmcnt(0)
	v_max_f32_e32 v100, v100, v100
	v_max_f32_e32 v101, v101, v101
	v_max_f32_e32 v102, v102, v102
	v_max_f32_e32 v103, v103, v103
	v_max_f32_e32 v104, v104, v104
	v_max_f32_e32 v105, v105, v105
	v_max_f32_e32 v106, v106, v106
	v_max_f32_e32 v107, v107, v107
	v_max_f32_e32 v108, v108, v108
	v_max_f32_e32 v109, v109, v109
	v_max_f32_e32 v110, v110, v110
	v_max_f32_e32 v111, v111, v111
	v_max_f32_e32 v112, v112, v112
	v_max_f32_e32 v113, v113, v113
	v_max_f32_e32 v114, v114, v114
	v_max_f32_e32 v115, v115, v115
	v_med3_f32 v100, v100, s20, v129
	v_med3_f32 v101, v101, s20, v129
	v_med3_f32 v102, v102, s20, v129
	v_med3_f32 v103, v103, s20, v129
	v_med3_f32 v104, v104, s20, v129
	v_med3_f32 v105, v105, s20, v129
	v_med3_f32 v106, v106, s20, v129
	v_med3_f32 v107, v107, s20, v129
	v_med3_f32 v108, v108, s20, v129
	v_med3_f32 v109, v109, s20, v129
	v_med3_f32 v110, v110, s20, v129
	v_med3_f32 v111, v111, s20, v129
	v_med3_f32 v112, v112, s20, v129
	v_med3_f32 v113, v113, s20, v129
	v_med3_f32 v114, v114, s20, v129
	v_med3_f32 v115, v115, s20, v129
	v_mov_b32_e32 v116, 0
	v_mov_b32_e32 v117, 0
	v_mov_b32_e32 v118, 0
	v_mov_b32_e32 v119, 0
	v_cvt_pk_fp8_f32 v116, v100, v101
	v_cvt_pk_fp8_f32 v117, v104, v105
	v_cvt_pk_fp8_f32 v118, v108, v109
	v_cvt_pk_fp8_f32 v119, v112, v113
	v_cvt_pk_fp8_f32 v116, v102, v103 op_sel:[0,0,1]
	v_cvt_pk_fp8_f32 v117, v106, v107 op_sel:[0,0,1]
	v_cvt_pk_fp8_f32 v118, v110, v111 op_sel:[0,0,1]
	v_cvt_pk_fp8_f32 v119, v114, v115 op_sel:[0,0,1]
	s_nop 0
	global_store_dwordx4 v128, v[116:119], s[14:15]
	s_waitcnt vmcnt(12)
	v_mul_f32_e32 v36, 0x43000000, v36
	v_mul_f32_e32 v37, 0x43000000, v37
	v_mul_f32_e32 v38, 0x43000000, v38
	v_mul_f32_e32 v39, 0x43000000, v39
	ds_write_b128 v120, v[36:39]
	v_mul_f32_e32 v40, 0x43000000, v40
	v_mul_f32_e32 v41, 0x43000000, v41
	v_mul_f32_e32 v42, 0x43000000, v42
	v_mul_f32_e32 v43, 0x43000000, v43
	ds_write_b128 v120, v[40:43] offset:1024
	v_mul_f32_e32 v44, 0x43000000, v44
	v_mul_f32_e32 v45, 0x43000000, v45
	v_mul_f32_e32 v46, 0x43000000, v46
	v_mul_f32_e32 v47, 0x43000000, v47
	ds_write_b128 v120, v[44:47] offset:2048
	v_mul_f32_e32 v48, 0x43000000, v48
	v_mul_f32_e32 v49, 0x43000000, v49
	v_mul_f32_e32 v50, 0x43000000, v50
	v_mul_f32_e32 v51, 0x43000000, v51
	ds_write_b128 v120, v[48:51] offset:3072
	v_mul_f32_e32 v52, 0x43000000, v52
	v_mul_f32_e32 v53, 0x43000000, v53
	v_mul_f32_e32 v54, 0x43000000, v54
	v_mul_f32_e32 v55, 0x43000000, v55
	ds_write_b128 v120, v[52:55] offset:4096
	v_mul_f32_e32 v56, 0x43000000, v56
	v_mul_f32_e32 v57, 0x43000000, v57
	v_mul_f32_e32 v58, 0x43000000, v58
	v_mul_f32_e32 v59, 0x43000000, v59
	ds_write_b128 v120, v[56:59] offset:5120
	v_mul_f32_e32 v60, 0x43000000, v60
	v_mul_f32_e32 v61, 0x43000000, v61
	v_mul_f32_e32 v62, 0x43000000, v62
	v_mul_f32_e32 v63, 0x43000000, v63
	ds_write_b128 v120, v[60:63] offset:6144
	v_mul_f32_e32 v64, 0x43000000, v64
	v_mul_f32_e32 v65, 0x43000000, v65
	v_mul_f32_e32 v66, 0x43000000, v66
	v_mul_f32_e32 v67, 0x43000000, v67
	ds_write_b128 v120, v[64:67] offset:7168
	s_waitcnt lgkmcnt(0)
	s_barrier
; #define GAS __attribute__((address_space(1)))
; #define LAS __attribute__((address_space(3)))
; #define LDS_WAIT() asm volatile("s_waitcnt lgkmcnt(0)" ::: "memory")
; __device__ __forceinline__ unsigned pk4_fp8(float a, float b, float c, float d) {
;     a = fminf(fmaxf(a, -448.f), 448.f); b = fminf(fmaxf(b, -448.f), 448.f); c = fminf(fmaxf(c, -448.f), 448.f); d = fminf(fmaxf(d, -448.f), 448.f);
;     int w = __builtin_amdgcn_cvt_pk_fp8_f32(a, b, 0, false); w = __builtin_amdgcn_cvt_pk_fp8_f32(c, d, w, true); return (unsigned)w; }
;     ...
;     for (int i = 0; i < 32; ++i) v[i] = sc >= 0 ? W[(size_t)(k0 + 2 * i + (lane >> 5)) * Nsrc + sc] : 0.f;
; #pragma unroll
;     for (int i = 0; i < 32; ++i) { const int k = k0 + 2 * i + (lane >> 5); float x = v[i] * wscale; if (KS) x *= (k < ksplit ? ksA[k] : ksB[k - ksplit]); scr[(2 * i + (lane >> 5)) * 33 + (lane & 31)] = x; }
;     LDS_WAIT(); asm volatile("" ::: "memory");
;     const int c = lane & 7;
; #pragma unroll
;     for (int j = 0; j < 4; ++j) { const int n = (lane >> 3) + 8 * j; const LAS float* s = scr + (8 * c) * 33 + n;
;         const unsigned long long o = (unsigned long long)pg8::pk4_fp8(s[0 * 33], s[1 * 33], s[2 * 33], s[3 * 33]) | ((unsigned long long)pg8::pk4_fp8(s[4 * 33], s[5 * 33], s[6 * 33], s[7 * 33]) << 32);
;         *(GAS unsigned long long*)(WT + (size_t)(n0 + n) * K + k0 + 8 * c) = o; }
	s_add_i32 s17, s16, 576
	s_min_u32 s17, s17, 0x3ff
	s_lshr_b32 s18, s17, 5
	s_add_i32 s18, s18, 32
	s_and_b32 s19, s17, 31
	s_lshl_b32 s18, s18, 21
	s_lshl_b32 s19, s19, 9
	s_add_u32 s18, s18, s19
	s_add_u32 s10, s2, s18
	s_addc_u32 s11, s3, 0
	global_load_dwordx4 v[36:39], v126, s[10:11]
	s_add_u32 s10, s10, 0x8000
	s_addc_u32 s11, s11, 0
	global_load_dwordx4 v[40:43], v126, s[10:11]
	s_add_u32 s10, s10, 0x8000
	s_addc_u32 s11, s11, 0
	global_load_dwordx4 v[44:47], v126, s[10:11]
	s_add_u32 s10, s10, 0x8000
	s_addc_u32 s11, s11, 0
	global_load_dwordx4 v[48:51], v126, s[10:11]
	s_add_u32 s10, s10, 0x8000
	s_addc_u32 s11, s11, 0
	global_load_dwordx4 v[52:55], v126, s[10:11]
	s_add_u32 s10, s10, 0x8000
	s_addc_u32 s11, s11, 0
	global_load_dwordx4 v[56:59], v126, s[10:11]
	s_add_u32 s10, s10, 0x8000
	s_addc_u32 s11, s11, 0
	global_load_dwordx4 v[60:63], v126, s[10:11]
	s_add_u32 s10, s10, 0x8000
	s_addc_u32 s11, s11, 0
	global_load_dwordx4 v[64:67], v126, s[10:11]
	s_add_i32 s17, s16, 384
	s_min_u32 s17, s17, 0x3ff
	s_lshr_b32 s18, s17, 5
	s_add_i32 s18, s18, 32
	s_and_b32 s19, s17, 31
	s_lshl_b32 s19, s19, 21
	s_lshl_b32 s18, s18, 7
	s_add_u32 s18, s18, s19
	s_add_u32 s14, s4, s18
	s_addc_u32 s15, s5, 0
	ds_read_b32 v100, v122
	ds_read_b32 v101, v122 offset:512
	ds_read_b32 v102, v122 offset:1024
	ds_read_b32 v103, v122 offset:1536
	ds_read_b32 v104, v122 offset:2048
	ds_read_b32 v105, v122 offset:2560
	ds_read_b32 v106, v122 offset:3072
	ds_read_b32 v107, v122 offset:3584
	ds_read_b32 v108, v122 offset:4096
	ds_read_b32 v109, v122 offset:4608
	ds_read_b32 v110, v122 offset:5120
	ds_read_b32 v111, v122 offset:5632
	ds_read_b32 v112, v122 offset:6144
	ds_read_b32 v113, v122 offset:6656
	ds_read_b32 v114, v122 offset:7168
	ds_read_b32 v115, v122 offset:7680
	s_waitcnt lgkmcnt(0)
	v_max_f32_e32 v100, v100, v100
	v_max_f32_e32 v101, v101, v101
	v_max_f32_e32 v102, v102, v102
	v_max_f32_e32 v103, v103, v103
	v_max_f32_e32 v104, v104, v104
	v_max_f32_e32 v105, v105, v105
	v_max_f32_e32 v106, v106, v106
	v_max_f32_e32 v107, v107, v107
	v_max_f32_e32 v108, v108, v108
	v_max_f32_e32 v109, v109, v109
	v_max_f32_e32 v110, v110, v110
	v_max_f32_e32 v111, v111, v111
	v_max_f32_e32 v112, v112, v112
	v_max_f32_e32 v113, v113, v113
	v_max_f32_e32 v114, v114, v114
	v_max_f32_e32 v115, v115, v115
	v_med3_f32 v100, v100, s20, v129
	v_med3_f32 v101, v101, s20, v129
	v_med3_f32 v102, v102, s20, v129
	v_med3_f32 v103, v103, s20, v129
	v_med3_f32 v104, v104, s20, v129
	v_med3_f32 v105, v105, s20, v129
	v_med3_f32 v106, v106, s20, v129
	v_med3_f32 v107, v107, s20, v129
	v_med3_f32 v108, v108, s20, v129
	v_med3_f32 v109, v109, s20, v129
	v_med3_f32 v110, v110, s20, v129
	v_med3_f32 v111, v111, s20, v129
	v_med3_f32 v112, v112, s20, v129
	v_med3_f32 v113, v113, s20, v129
	v_med3_f32 v114, v114, s20, v129
	v_med3_f32 v115, v115, s20, v129
	v_mov_b32_e32 v116, 0
	v_mov_b32_e32 v117, 0
	v_mov_b32_e32 v118, 0
	v_mov_b32_e32 v119, 0
	v_cvt_pk_fp8_f32 v116, v100, v101
	v_cvt_pk_fp8_f32 v117, v104, v105
	v_cvt_pk_fp8_f32 v118, v108, v109
	v_cvt_pk_fp8_f32 v119, v112, v113
	v_cvt_pk_fp8_f32 v116, v102, v103 op_sel:[0,0,1]
	v_cvt_pk_fp8_f32 v117, v106, v107 op_sel:[0,0,1]
	v_cvt_pk_fp8_f32 v118, v110, v111 op_sel:[0,0,1]
	v_cvt_pk_fp8_f32 v119, v114, v115 op_sel:[0,0,1]
	s_nop 0
	global_store_dwordx4 v127, v[116:119], s[14:15]
	ds_read_b32 v100, v124
	ds_read_b32 v101, v124 offset:512
	ds_read_b32 v102, v124 offset:1024
	ds_read_b32 v103, v124 offset:1536
	ds_read_b32 v104, v124 offset:2048
	ds_read_b32 v105, v124 offset:2560
	ds_read_b32 v106, v124 offset:3072
	ds_read_b32 v107, v124 offset:3584
	ds_read_b32 v108, v124 offset:4096
	ds_read_b32 v109, v124 offset:4608
	ds_read_b32 v110, v124 offset:5120
	ds_read_b32 v111, v124 offset:5632
	ds_read_b32 v112, v124 offset:6144
	ds_read_b32 v113, v124 offset:6656
	ds_read_b32 v114, v124 offset:7168
	ds_read_b32 v115, v124 offset:7680
	s_waitcnt lgkmcnt(0)
	v_max_f32_e32 v100, v100, v100
	v_max_f32_e32 v101, v101, v101
	v_max_f32_e32 v102, v102, v102
	v_max_f32_e32 v103, v103, v103
	v_max_f32_e32 v104, v104, v104
	v_max_f32_e32 v105, v105, v105
	v_max_f32_e32 v106, v106, v106
	v_max_f32_e32 v107, v107, v107
	v_max_f32_e32 v108, v108, v108
	v_max_f32_e32 v109, v109, v109
	v_max_f32_e32 v110, v110, v110
	v_max_f32_e32 v111, v111, v111
	v_max_f32_e32 v112, v112, v112
	v_max_f32_e32 v113, v113, v113
	v_max_f32_e32 v114, v114, v114
	v_max_f32_e32 v115, v115, v115
	v_med3_f32 v100, v100, s20, v129
	v_med3_f32 v101, v101, s20, v129
	v_med3_f32 v102, v102, s20, v129
	v_med3_f32 v103, v103, s20, v129
	v_med3_f32 v104, v104, s20, v129
	v_med3_f32 v105, v105, s20, v129
	v_med3_f32 v106, v106, s20, v129
	v_med3_f32 v107, v107, s20, v129
	v_med3_f32 v108, v108, s20, v129
	v_med3_f32 v109, v109, s20, v129
	v_med3_f32 v110, v110, s20, v129
	v_med3_f32 v111, v111, s20, v129
	v_med3_f32 v112, v112, s20, v129
	v_med3_f32 v113, v113, s20, v129
	v_med3_f32 v114, v114, s20, v129
	v_med3_f32 v115, v115, s20, v129
	v_mov_b32_e32 v116, 0
	v_mov_b32_e32 v117, 0
	v_mov_b32_e32 v118, 0
	v_mov_b32_e32 v119, 0
	v_cvt_pk_fp8_f32 v116, v100, v101
	v_cvt_pk_fp8_f32 v117, v104, v105
	v_cvt_pk_fp8_f32 v118, v108, v109
	v_cvt_pk_fp8_f32 v119, v112, v113
	v_cvt_pk_fp8_f32 v116, v102, v103 op_sel:[0,0,1]
	v_cvt_pk_fp8_f32 v117, v106, v107 op_sel:[0,0,1]
	v_cvt_pk_fp8_f32 v118, v110, v111 op_sel:[0,0,1]
	v_cvt_pk_fp8_f32 v119, v114, v115 op_sel:[0,0,1]
	s_nop 0
	global_store_dwordx4 v128, v[116:119], s[14:15]
	s_waitcnt vmcnt(12)
	v_mul_f32_e32 v68, 0x43000000, v68
	v_mul_f32_e32 v69, 0x43000000, v69
	v_mul_f32_e32 v70, 0x43000000, v70
	v_mul_f32_e32 v71, 0x43000000, v71
	ds_write_b128 v121, v[68:71]
	v_mul_f32_e32 v72, 0x43000000, v72
	v_mul_f32_e32 v73, 0x43000000, v73
	v_mul_f32_e32 v74, 0x43000000, v74
	v_mul_f32_e32 v75, 0x43000000, v75
	ds_write_b128 v121, v[72:75] offset:1024
	v_mul_f32_e32 v76, 0x43000000, v76
	v_mul_f32_e32 v77, 0x43000000, v77
	v_mul_f32_e32 v78, 0x43000000, v78
	v_mul_f32_e32 v79, 0x43000000, v79
	ds_write_b128 v121, v[76:79] offset:2048
	v_mul_f32_e32 v80, 0x43000000, v80
	v_mul_f32_e32 v81, 0x43000000, v81
	v_mul_f32_e32 v82, 0x43000000, v82
	v_mul_f32_e32 v83, 0x43000000, v83
	ds_write_b128 v121, v[80:83] offset:3072
	v_mul_f32_e32 v84, 0x43000000, v84
	v_mul_f32_e32 v85, 0x43000000, v85
	v_mul_f32_e32 v86, 0x43000000, v86
	v_mul_f32_e32 v87, 0x43000000, v87
	ds_write_b128 v121, v[84:87] offset:4096
	v_mul_f32_e32 v88, 0x43000000, v88
	v_mul_f32_e32 v89, 0x43000000, v89
	v_mul_f32_e32 v90, 0x43000000, v90
	v_mul_f32_e32 v91, 0x43000000, v91
	ds_write_b128 v121, v[88:91] offset:5120
	v_mul_f32_e32 v92, 0x43000000, v92
	v_mul_f32_e32 v93, 0x43000000, v93
	v_mul_f32_e32 v94, 0x43000000, v94
	v_mul_f32_e32 v95, 0x43000000, v95
	ds_write_b128 v121, v[92:95] offset:6144
	v_mul_f32_e32 v96, 0x43000000, v96
	v_mul_f32_e32 v97, 0x43000000, v97
	v_mul_f32_e32 v98, 0x43000000, v98
	v_mul_f32_e32 v99, 0x43000000, v99
	ds_write_b128 v121, v[96:99] offset:7168
	s_waitcnt lgkmcnt(0)
	s_barrier
; #define GAS __attribute__((address_space(1)))
; #define LAS __attribute__((address_space(3)))
; #define LDS_WAIT() asm volatile("s_waitcnt lgkmcnt(0)" ::: "memory")
; __device__ __forceinline__ unsigned pk4_fp8(float a, float b, float c, float d) {
;     a = fminf(fmaxf(a, -448.f), 448.f); b = fminf(fmaxf(b, -448.f), 448.f); c = fminf(fmaxf(c, -448.f), 448.f); d = fminf(fmaxf(d, -448.f), 448.f);
;     int w = __builtin_amdgcn_cvt_pk_fp8_f32(a, b, 0, false); w = __builtin_amdgcn_cvt_pk_fp8_f32(c, d, w, true); return (unsigned)w; }
;     ...
;     for (int i = 0; i < 32; ++i) v[i] = sc >= 0 ? W[(size_t)(k0 + 2 * i + (lane >> 5)) * Nsrc + sc] : 0.f;
; #pragma unroll
;     for (int i = 0; i < 32; ++i) { const int k = k0 + 2 * i + (lane >> 5); float x = v[i] * wscale; if (KS) x *= (k < ksplit ? ksA[k] : ksB[k - ksplit]); scr[(2 * i + (lane >> 5)) * 33 + (lane & 31)] = x; }
;     LDS_WAIT(); asm volatile("" ::: "memory");
;     const int c = lane & 7;
; #pragma unroll
;     for (int j = 0; j < 4; ++j) { const int n = (lane >> 3) + 8 * j; const LAS float* s = scr + (8 * c) * 33 + n;
;         const unsigned long long o = (unsigned long long)pg8::pk4_fp8(s[0 * 33], s[1 * 33], s[2 * 33], s[3 * 33]) | ((unsigned long long)pg8::pk4_fp8(s[4 * 33], s[5 * 33], s[6 * 33], s[7 * 33]) << 32);
;         *(GAS unsigned long long*)(WT + (size_t)(n0 + n) * K + k0 + 8 * c) = o; }
	s_add_i32 s17, s16, 672
	s_min_u32 s17, s17, 0x3ff
	s_lshr_b32 s18, s17, 5
	s_add_i32 s18, s18, 32
	s_and_b32 s19, s17, 31
	s_lshl_b32 s18, s18, 21
	s_lshl_b32 s19, s19, 9
	s_add_u32 s18, s18, s19
	s_add_u32 s10, s2, s18
	s_addc_u32 s11, s3, 0
	global_load_dwordx4 v[68:71], v126, s[10:11]
	s_add_u32 s10, s10, 0x8000
	s_addc_u32 s11, s11, 0
	global_load_dwordx4 v[72:75], v126, s[10:11]
	s_add_u32 s10, s10, 0x8000
	s_addc_u32 s11, s11, 0
	global_load_dwordx4 v[76:79], v126, s[10:11]
	s_add_u32 s10, s10, 0x8000
	s_addc_u32 s11, s11, 0
	global_load_dwordx4 v[80:83], v126, s[10:11]
	s_add_u32 s10, s10, 0x8000
	s_addc_u32 s11, s11, 0
	global_load_dwordx4 v[84:87], v126, s[10:11]
	s_add_u32 s10, s10, 0x8000
	s_addc_u32 s11, s11, 0
	global_load_dwordx4 v[88:91], v126, s[10:11]
	s_add_u32 s10, s10, 0x8000
	s_addc_u32 s11, s11, 0
	global_load_dwordx4 v[92:95], v126, s[10:11]
	s_add_u32 s10, s10, 0x8000
	s_addc_u32 s11, s11, 0
	global_load_dwordx4 v[96:99], v126, s[10:11]
	s_add_i32 s17, s16, 480
	s_min_u32 s17, s17, 0x3ff
	s_lshr_b32 s18, s17, 5
	s_add_i32 s18, s18, 32
	s_and_b32 s19, s17, 31
	s_lshl_b32 s19, s19, 21
	s_lshl_b32 s18, s18, 7
	s_add_u32 s18, s18, s19
	s_add_u32 s14, s4, s18
	s_addc_u32 s15, s5, 0
	ds_read_b32 v100, v123
	ds_read_b32 v101, v123 offset:512
	ds_read_b32 v102, v123 offset:1024
	ds_read_b32 v103, v123 offset:1536
	ds_read_b32 v104, v123 offset:2048
	ds_read_b32 v105, v123 offset:2560
	ds_read_b32 v106, v123 offset:3072
	ds_read_b32 v107, v123 offset:3584
	ds_read_b32 v108, v123 offset:4096
	ds_read_b32 v109, v123 offset:4608
	ds_read_b32 v110, v123 offset:5120
	ds_read_b32 v111, v123 offset:5632
	ds_read_b32 v112, v123 offset:6144
	ds_read_b32 v113, v123 offset:6656
	ds_read_b32 v114, v123 offset:7168
	ds_read_b32 v115, v123 offset:7680
	s_waitcnt lgkmcnt(0)
	v_max_f32_e32 v100, v100, v100
	v_max_f32_e32 v101, v101, v101
	v_max_f32_e32 v102, v102, v102
	v_max_f32_e32 v103, v103, v103
	v_max_f32_e32 v104, v104, v104
	v_max_f32_e32 v105, v105, v105
	v_max_f32_e32 v106, v106, v106
	v_max_f32_e32 v107, v107, v107
	v_max_f32_e32 v108, v108, v108
	v_max_f32_e32 v109, v109, v109
	v_max_f32_e32 v110, v110, v110
	v_max_f32_e32 v111, v111, v111
	v_max_f32_e32 v112, v112, v112
	v_max_f32_e32 v113, v113, v113
	v_max_f32_e32 v114, v114, v114
	v_max_f32_e32 v115, v115, v115
	v_med3_f32 v100, v100, s20, v129
	v_med3_f32 v101, v101, s20, v129
	v_med3_f32 v102, v102, s20, v129
	v_med3_f32 v103, v103, s20, v129
	v_med3_f32 v104, v104, s20, v129
	v_med3_f32 v105, v105, s20, v129
	v_med3_f32 v106, v106, s20, v129
	v_med3_f32 v107, v107, s20, v129
	v_med3_f32 v108, v108, s20, v129
	v_med3_f32 v109, v109, s20, v129
	v_med3_f32 v110, v110, s20, v129
	v_med3_f32 v111, v111, s20, v129
	v_med3_f32 v112, v112, s20, v129
	v_med3_f32 v113, v113, s20, v129
	v_med3_f32 v114, v114, s20, v129
	v_med3_f32 v115, v115, s20, v129
	v_mov_b32_e32 v116, 0
	v_mov_b32_e32 v117, 0
	v_mov_b32_e32 v118, 0
	v_mov_b32_e32 v119, 0
	v_cvt_pk_fp8_f32 v116, v100, v101
	v_cvt_pk_fp8_f32 v117, v104, v105
	v_cvt_pk_fp8_f32 v118, v108, v109
	v_cvt_pk_fp8_f32 v119, v112, v113
	v_cvt_pk_fp8_f32 v116, v102, v103 op_sel:[0,0,1]
	v_cvt_pk_fp8_f32 v117, v106, v107 op_sel:[0,0,1]
	v_cvt_pk_fp8_f32 v118, v110, v111 op_sel:[0,0,1]
	v_cvt_pk_fp8_f32 v119, v114, v115 op_sel:[0,0,1]
	s_nop 0
	global_store_dwordx4 v127, v[116:119], s[14:15]
	ds_read_b32 v100, v125
	ds_read_b32 v101, v125 offset:512
	ds_read_b32 v102, v125 offset:1024
	ds_read_b32 v103, v125 offset:1536
	ds_read_b32 v104, v125 offset:2048
	ds_read_b32 v105, v125 offset:2560
	ds_read_b32 v106, v125 offset:3072
	ds_read_b32 v107, v125 offset:3584
	ds_read_b32 v108, v125 offset:4096
	ds_read_b32 v109, v125 offset:4608
	ds_read_b32 v110, v125 offset:5120
	ds_read_b32 v111, v125 offset:5632
	ds_read_b32 v112, v125 offset:6144
	ds_read_b32 v113, v125 offset:6656
	ds_read_b32 v114, v125 offset:7168
	ds_read_b32 v115, v125 offset:7680
	s_waitcnt lgkmcnt(0)
	v_max_f32_e32 v100, v100, v100
	v_max_f32_e32 v101, v101, v101
	v_max_f32_e32 v102, v102, v102
	v_max_f32_e32 v103, v103, v103
	v_max_f32_e32 v104, v104, v104
	v_max_f32_e32 v105, v105, v105
	v_max_f32_e32 v106, v106, v106
	v_max_f32_e32 v107, v107, v107
	v_max_f32_e32 v108, v108, v108
	v_max_f32_e32 v109, v109, v109
	v_max_f32_e32 v110, v110, v110
	v_max_f32_e32 v111, v111, v111
	v_max_f32_e32 v112, v112, v112
	v_max_f32_e32 v113, v113, v113
	v_max_f32_e32 v114, v114, v114
	v_max_f32_e32 v115, v115, v115
	v_med3_f32 v100, v100, s20, v129
	v_med3_f32 v101, v101, s20, v129
	v_med3_f32 v102, v102, s20, v129
	v_med3_f32 v103, v103, s20, v129
	v_med3_f32 v104, v104, s20, v129
	v_med3_f32 v105, v105, s20, v129
	v_med3_f32 v106, v106, s20, v129
	v_med3_f32 v107, v107, s20, v129
	v_med3_f32 v108, v108, s20, v129
	v_med3_f32 v109, v109, s20, v129
	v_med3_f32 v110, v110, s20, v129
	v_med3_f32 v111, v111, s20, v129
	v_med3_f32 v112, v112, s20, v129
	v_med3_f32 v113, v113, s20, v129
	v_med3_f32 v114, v114, s20, v129
	v_med3_f32 v115, v115, s20, v129
	v_mov_b32_e32 v116, 0
	v_mov_b32_e32 v117, 0
	v_mov_b32_e32 v118, 0
	v_mov_b32_e32 v119, 0
	v_cvt_pk_fp8_f32 v116, v100, v101
	v_cvt_pk_fp8_f32 v117, v104, v105
	v_cvt_pk_fp8_f32 v118, v108, v109
	v_cvt_pk_fp8_f32 v119, v112, v113
	v_cvt_pk_fp8_f32 v116, v102, v103 op_sel:[0,0,1]
	v_cvt_pk_fp8_f32 v117, v106, v107 op_sel:[0,0,1]
	v_cvt_pk_fp8_f32 v118, v110, v111 op_sel:[0,0,1]
	v_cvt_pk_fp8_f32 v119, v114, v115 op_sel:[0,0,1]
	s_nop 0
	global_store_dwordx4 v128, v[116:119], s[14:15]
	s_waitcnt vmcnt(12)
	v_mul_f32_e32 v36, 0x43000000, v36
	v_mul_f32_e32 v37, 0x43000000, v37
	v_mul_f32_e32 v38, 0x43000000, v38
	v_mul_f32_e32 v39, 0x43000000, v39
	ds_write_b128 v120, v[36:39]
	v_mul_f32_e32 v40, 0x43000000, v40
	v_mul_f32_e32 v41, 0x43000000, v41
	v_mul_f32_e32 v42, 0x43000000, v42
	v_mul_f32_e32 v43, 0x43000000, v43
	ds_write_b128 v120, v[40:43] offset:1024
	v_mul_f32_e32 v44, 0x43000000, v44
	v_mul_f32_e32 v45, 0x43000000, v45
	v_mul_f32_e32 v46, 0x43000000, v46
	v_mul_f32_e32 v47, 0x43000000, v47
	ds_write_b128 v120, v[44:47] offset:2048
	v_mul_f32_e32 v48, 0x43000000, v48
	v_mul_f32_e32 v49, 0x43000000, v49
	v_mul_f32_e32 v50, 0x43000000, v50
	v_mul_f32_e32 v51, 0x43000000, v51
	ds_write_b128 v120, v[48:51] offset:3072
	v_mul_f32_e32 v52, 0x43000000, v52
	v_mul_f32_e32 v53, 0x43000000, v53
	v_mul_f32_e32 v54, 0x43000000, v54
	v_mul_f32_e32 v55, 0x43000000, v55
	ds_write_b128 v120, v[52:55] offset:4096
	v_mul_f32_e32 v56, 0x43000000, v56
	v_mul_f32_e32 v57, 0x43000000, v57
	v_mul_f32_e32 v58, 0x43000000, v58
	v_mul_f32_e32 v59, 0x43000000, v59
	ds_write_b128 v120, v[56:59] offset:5120
	v_mul_f32_e32 v60, 0x43000000, v60
	v_mul_f32_e32 v61, 0x43000000, v61
	v_mul_f32_e32 v62, 0x43000000, v62
	v_mul_f32_e32 v63, 0x43000000, v63
	ds_write_b128 v120, v[60:63] offset:6144
	v_mul_f32_e32 v64, 0x43000000, v64
	v_mul_f32_e32 v65, 0x43000000, v65
	v_mul_f32_e32 v66, 0x43000000, v66
	v_mul_f32_e32 v67, 0x43000000, v67
	ds_write_b128 v120, v[64:67] offset:7168
	s_waitcnt lgkmcnt(0)
	s_barrier
; #define GAS __attribute__((address_space(1)))
; #define LAS __attribute__((address_space(3)))
; #define LDS_WAIT() asm volatile("s_waitcnt lgkmcnt(0)" ::: "memory")
; __device__ __forceinline__ unsigned pk4_fp8(float a, float b, float c, float d) {
;     a = fminf(fmaxf(a, -448.f), 448.f); b = fminf(fmaxf(b, -448.f), 448.f); c = fminf(fmaxf(c, -448.f), 448.f); d = fminf(fmaxf(d, -448.f), 448.f);
;     int w = __builtin_amdgcn_cvt_pk_fp8_f32(a, b, 0, false); w = __builtin_amdgcn_cvt_pk_fp8_f32(c, d, w, true); return (unsigned)w; }
;     ...
;     for (int i = 0; i < 32; ++i) v[i] = sc >= 0 ? W[(size_t)(k0 + 2 * i + (lane >> 5)) * Nsrc + sc] : 0.f;
; #pragma unroll
;     for (int i = 0; i < 32; ++i) { const int k = k0 + 2 * i + (lane >> 5); float x = v[i] * wscale; if (KS) x *= (k < ksplit ? ksA[k] : ksB[k - ksplit]); scr[(2 * i + (lane >> 5)) * 33 + (lane & 31)] = x; }
;     LDS_WAIT(); asm volatile("" ::: "memory");
;     const int c = lane & 7;
; #pragma unroll
;     for (int j = 0; j < 4; ++j) { const int n = (lane >> 3) + 8 * j; const LAS float* s = scr + (8 * c) * 33 + n;
;         const unsigned long long o = (unsigned long long)pg8::pk4_fp8(s[0 * 33], s[1 * 33], s[2 * 33], s[3 * 33]) | ((unsigned long long)pg8::pk4_fp8(s[4 * 33], s[5 * 33], s[6 * 33], s[7 * 33]) << 32);
;         *(GAS unsigned long long*)(WT + (size_t)(n0 + n) * K + k0 + 8 * c) = o; }
	s_add_i32 s17, s16, 768
	s_min_u32 s17, s17, 0x3ff
	s_lshr_b32 s18, s17, 5
	s_add_i32 s18, s18, 32
	s_and_b32 s19, s17, 31
	s_lshl_b32 s18, s18, 21
	s_lshl_b32 s19, s19, 9
	s_add_u32 s18, s18, s19
	s_add_u32 s10, s2, s18
	s_addc_u32 s11, s3, 0
	global_load_dwordx4 v[36:39], v126, s[10:11]
	s_add_u32 s10, s10, 0x8000
	s_addc_u32 s11, s11, 0
	global_load_dwordx4 v[40:43], v126, s[10:11]
	s_add_u32 s10, s10, 0x8000
	s_addc_u32 s11, s11, 0
	global_load_dwordx4 v[44:47], v126, s[10:11]
	s_add_u32 s10, s10, 0x8000
	s_addc_u32 s11, s11, 0
	global_load_dwordx4 v[48:51], v126, s[10:11]
	s_add_u32 s10, s10, 0x8000
	s_addc_u32 s11, s11, 0
	global_load_dwordx4 v[52:55], v126, s[10:11]
	s_add_u32 s10, s10, 0x8000
	s_addc_u32 s11, s11, 0
	global_load_dwordx4 v[56:59], v126, s[10:11]
	s_add_u32 s10, s10, 0x8000
	s_addc_u32 s11, s11, 0
	global_load_dwordx4 v[60:63], v126, s[10:11]
	s_add_u32 s10, s10, 0x8000
	s_addc_u32 s11, s11, 0
	global_load_dwordx4 v[64:67], v126, s[10:11]
	s_add_i32 s17, s16, 576
	s_min_u32 s17, s17, 0x3ff
	s_lshr_b32 s18, s17, 5
	s_add_i32 s18, s18, 32
	s_and_b32 s19, s17, 31
	s_lshl_b32 s19, s19, 21
	s_lshl_b32 s18, s18, 7
	s_add_u32 s18, s18, s19
	s_add_u32 s14, s4, s18
	s_addc_u32 s15, s5, 0
	ds_read_b32 v100, v122
	ds_read_b32 v101, v122 offset:512
	ds_read_b32 v102, v122 offset:1024
	ds_read_b32 v103, v122 offset:1536
	ds_read_b32 v104, v122 offset:2048
	ds_read_b32 v105, v122 offset:2560
	ds_read_b32 v106, v122 offset:3072
	ds_read_b32 v107, v122 offset:3584
	ds_read_b32 v108, v122 offset:4096
	ds_read_b32 v109, v122 offset:4608
	ds_read_b32 v110, v122 offset:5120
	ds_read_b32 v111, v122 offset:5632
	ds_read_b32 v112, v122 offset:6144
	ds_read_b32 v113, v122 offset:6656
	ds_read_b32 v114, v122 offset:7168
	ds_read_b32 v115, v122 offset:7680
	s_waitcnt lgkmcnt(0)
	v_max_f32_e32 v100, v100, v100
	v_max_f32_e32 v101, v101, v101
	v_max_f32_e32 v102, v102, v102
	v_max_f32_e32 v103, v103, v103
	v_max_f32_e32 v104, v104, v104
	v_max_f32_e32 v105, v105, v105
	v_max_f32_e32 v106, v106, v106
	v_max_f32_e32 v107, v107, v107
	v_max_f32_e32 v108, v108, v108
	v_max_f32_e32 v109, v109, v109
	v_max_f32_e32 v110, v110, v110
	v_max_f32_e32 v111, v111, v111
	v_max_f32_e32 v112, v112, v112
	v_max_f32_e32 v113, v113, v113
	v_max_f32_e32 v114, v114, v114
	v_max_f32_e32 v115, v115, v115
	v_med3_f32 v100, v100, s20, v129
	v_med3_f32 v101, v101, s20, v129
	v_med3_f32 v102, v102, s20, v129
	v_med3_f32 v103, v103, s20, v129
	v_med3_f32 v104, v104, s20, v129
	v_med3_f32 v105, v105, s20, v129
	v_med3_f32 v106, v106, s20, v129
	v_med3_f32 v107, v107, s20, v129
	v_med3_f32 v108, v108, s20, v129
	v_med3_f32 v109, v109, s20, v129
	v_med3_f32 v110, v110, s20, v129
	v_med3_f32 v111, v111, s20, v129
	v_med3_f32 v112, v112, s20, v129
	v_med3_f32 v113, v113, s20, v129
	v_med3_f32 v114, v114, s20, v129
	v_med3_f32 v115, v115, s20, v129
	v_mov_b32_e32 v116, 0
	v_mov_b32_e32 v117, 0
	v_mov_b32_e32 v118, 0
	v_mov_b32_e32 v119, 0
	v_cvt_pk_fp8_f32 v116, v100, v101
	v_cvt_pk_fp8_f32 v117, v104, v105
	v_cvt_pk_fp8_f32 v118, v108, v109
	v_cvt_pk_fp8_f32 v119, v112, v113
	v_cvt_pk_fp8_f32 v116, v102, v103 op_sel:[0,0,1]
	v_cvt_pk_fp8_f32 v117, v106, v107 op_sel:[0,0,1]
	v_cvt_pk_fp8_f32 v118, v110, v111 op_sel:[0,0,1]
	v_cvt_pk_fp8_f32 v119, v114, v115 op_sel:[0,0,1]
	s_nop 0
	global_store_dwordx4 v127, v[116:119], s[14:15]
	ds_read_b32 v100, v124
	ds_read_b32 v101, v124 offset:512
	ds_read_b32 v102, v124 offset:1024
	ds_read_b32 v103, v124 offset:1536
	ds_read_b32 v104, v124 offset:2048
	ds_read_b32 v105, v124 offset:2560
	ds_read_b32 v106, v124 offset:3072
	ds_read_b32 v107, v124 offset:3584
	ds_read_b32 v108, v124 offset:4096
	ds_read_b32 v109, v124 offset:4608
	ds_read_b32 v110, v124 offset:5120
	ds_read_b32 v111, v124 offset:5632
	ds_read_b32 v112, v124 offset:6144
	ds_read_b32 v113, v124 offset:6656
	ds_read_b32 v114, v124 offset:7168
	ds_read_b32 v115, v124 offset:7680
	s_waitcnt lgkmcnt(0)
	v_max_f32_e32 v100, v100, v100
	v_max_f32_e32 v101, v101, v101
	v_max_f32_e32 v102, v102, v102
	v_max_f32_e32 v103, v103, v103
	v_max_f32_e32 v104, v104, v104
	v_max_f32_e32 v105, v105, v105
	v_max_f32_e32 v106, v106, v106
	v_max_f32_e32 v107, v107, v107
	v_max_f32_e32 v108, v108, v108
	v_max_f32_e32 v109, v109, v109
	v_max_f32_e32 v110, v110, v110
	v_max_f32_e32 v111, v111, v111
	v_max_f32_e32 v112, v112, v112
	v_max_f32_e32 v113, v113, v113
	v_max_f32_e32 v114, v114, v114
	v_max_f32_e32 v115, v115, v115
	v_med3_f32 v100, v100, s20, v129
	v_med3_f32 v101, v101, s20, v129
	v_med3_f32 v102, v102, s20, v129
	v_med3_f32 v103, v103, s20, v129
	v_med3_f32 v104, v104, s20, v129
	v_med3_f32 v105, v105, s20, v129
	v_med3_f32 v106, v106, s20, v129
	v_med3_f32 v107, v107, s20, v129
	v_med3_f32 v108, v108, s20, v129
	v_med3_f32 v109, v109, s20, v129
	v_med3_f32 v110, v110, s20, v129
	v_med3_f32 v111, v111, s20, v129
	v_med3_f32 v112, v112, s20, v129
	v_med3_f32 v113, v113, s20, v129
	v_med3_f32 v114, v114, s20, v129
	v_med3_f32 v115, v115, s20, v129
	v_mov_b32_e32 v116, 0
	v_mov_b32_e32 v117, 0
	v_mov_b32_e32 v118, 0
	v_mov_b32_e32 v119, 0
	v_cvt_pk_fp8_f32 v116, v100, v101
	v_cvt_pk_fp8_f32 v117, v104, v105
	v_cvt_pk_fp8_f32 v118, v108, v109
	v_cvt_pk_fp8_f32 v119, v112, v113
	v_cvt_pk_fp8_f32 v116, v102, v103 op_sel:[0,0,1]
	v_cvt_pk_fp8_f32 v117, v106, v107 op_sel:[0,0,1]
	v_cvt_pk_fp8_f32 v118, v110, v111 op_sel:[0,0,1]
	v_cvt_pk_fp8_f32 v119, v114, v115 op_sel:[0,0,1]
	s_nop 0
	global_store_dwordx4 v128, v[116:119], s[14:15]
	s_waitcnt vmcnt(12)
	v_mul_f32_e32 v68, 0x43000000, v68
	v_mul_f32_e32 v69, 0x43000000, v69
	v_mul_f32_e32 v70, 0x43000000, v70
	v_mul_f32_e32 v71, 0x43000000, v71
	ds_write_b128 v121, v[68:71]
	v_mul_f32_e32 v72, 0x43000000, v72
	v_mul_f32_e32 v73, 0x43000000, v73
	v_mul_f32_e32 v74, 0x43000000, v74
	v_mul_f32_e32 v75, 0x43000000, v75
	ds_write_b128 v121, v[72:75] offset:1024
	v_mul_f32_e32 v76, 0x43000000, v76
	v_mul_f32_e32 v77, 0x43000000, v77
	v_mul_f32_e32 v78, 0x43000000, v78
	v_mul_f32_e32 v79, 0x43000000, v79
	ds_write_b128 v121, v[76:79] offset:2048
	v_mul_f32_e32 v80, 0x43000000, v80
	v_mul_f32_e32 v81, 0x43000000, v81
	v_mul_f32_e32 v82, 0x43000000, v82
	v_mul_f32_e32 v83, 0x43000000, v83
	ds_write_b128 v121, v[80:83] offset:3072
	v_mul_f32_e32 v84, 0x43000000, v84
	v_mul_f32_e32 v85, 0x43000000, v85
	v_mul_f32_e32 v86, 0x43000000, v86
	v_mul_f32_e32 v87, 0x43000000, v87
	ds_write_b128 v121, v[84:87] offset:4096
	v_mul_f32_e32 v88, 0x43000000, v88
	v_mul_f32_e32 v89, 0x43000000, v89
	v_mul_f32_e32 v90, 0x43000000, v90
	v_mul_f32_e32 v91, 0x43000000, v91
	ds_write_b128 v121, v[88:91] offset:5120
	v_mul_f32_e32 v92, 0x43000000, v92
	v_mul_f32_e32 v93, 0x43000000, v93
	v_mul_f32_e32 v94, 0x43000000, v94
	v_mul_f32_e32 v95, 0x43000000, v95
	ds_write_b128 v121, v[92:95] offset:6144
	v_mul_f32_e32 v96, 0x43000000, v96
	v_mul_f32_e32 v97, 0x43000000, v97
	v_mul_f32_e32 v98, 0x43000000, v98
	v_mul_f32_e32 v99, 0x43000000, v99
	ds_write_b128 v121, v[96:99] offset:7168
	s_waitcnt lgkmcnt(0)
	s_barrier
; #define GAS __attribute__((address_space(1)))
; #define LAS __attribute__((address_space(3)))
; #define LDS_WAIT() asm volatile("s_waitcnt lgkmcnt(0)" ::: "memory")
; __device__ __forceinline__ unsigned pk4_fp8(float a, float b, float c, float d) {
;     a = fminf(fmaxf(a, -448.f), 448.f); b = fminf(fmaxf(b, -448.f), 448.f); c = fminf(fmaxf(c, -448.f), 448.f); d = fminf(fmaxf(d, -448.f), 448.f);
;     int w = __builtin_amdgcn_cvt_pk_fp8_f32(a, b, 0, false); w = __builtin_amdgcn_cvt_pk_fp8_f32(c, d, w, true); return (unsigned)w; }
;     ...
;     for (int i = 0; i < 32; ++i) v[i] = sc >= 0 ? W[(size_t)(k0 + 2 * i + (lane >> 5)) * Nsrc + sc] : 0.f;
; #pragma unroll
;     for (int i = 0; i < 32; ++i) { const int k = k0 + 2 * i + (lane >> 5); float x = v[i] * wscale; if (KS) x *= (k < ksplit ? ksA[k] : ksB[k - ksplit]); scr[(2 * i + (lane >> 5)) * 33 + (lane & 31)] = x; }
;     LDS_WAIT(); asm volatile("" ::: "memory");
;     const int c = lane & 7;
; #pragma unroll
;     for (int j = 0; j < 4; ++j) { const int n = (lane >> 3) + 8 * j; const LAS float* s = scr + (8 * c) * 33 + n;
;         const unsigned long long o = (unsigned long long)pg8::pk4_fp8(s[0 * 33], s[1 * 33], s[2 * 33], s[3 * 33]) | ((unsigned long long)pg8::pk4_fp8(s[4 * 33], s[5 * 33], s[6 * 33], s[7 * 33]) << 32);
;         *(GAS unsigned long long*)(WT + (size_t)(n0 + n) * K + k0 + 8 * c) = o; }
	s_add_i32 s17, s16, 864
	s_min_u32 s17, s17, 0x3ff
	s_lshr_b32 s18, s17, 5
	s_add_i32 s18, s18, 32
	s_and_b32 s19, s17, 31
	s_lshl_b32 s18, s18, 21
	s_lshl_b32 s19, s19, 9
	s_add_u32 s18, s18, s19
	s_add_u32 s10, s2, s18
	s_addc_u32 s11, s3, 0
	global_load_dwordx4 v[68:71], v126, s[10:11]
	s_add_u32 s10, s10, 0x8000
	s_addc_u32 s11, s11, 0
	global_load_dwordx4 v[72:75], v126, s[10:11]
	s_add_u32 s10, s10, 0x8000
	s_addc_u32 s11, s11, 0
	global_load_dwordx4 v[76:79], v126, s[10:11]
	s_add_u32 s10, s10, 0x8000
	s_addc_u32 s11, s11, 0
	global_load_dwordx4 v[80:83], v126, s[10:11]
	s_add_u32 s10, s10, 0x8000
	s_addc_u32 s11, s11, 0
	global_load_dwordx4 v[84:87], v126, s[10:11]
	s_add_u32 s10, s10, 0x8000
	s_addc_u32 s11, s11, 0
	global_load_dwordx4 v[88:91], v126, s[10:11]
	s_add_u32 s10, s10, 0x8000
	s_addc_u32 s11, s11, 0
	global_load_dwordx4 v[92:95], v126, s[10:11]
	s_add_u32 s10, s10, 0x8000
	s_addc_u32 s11, s11, 0
	global_load_dwordx4 v[96:99], v126, s[10:11]
	s_add_i32 s17, s16, 672
	s_min_u32 s17, s17, 0x3ff
	s_lshr_b32 s18, s17, 5
	s_add_i32 s18, s18, 32
	s_and_b32 s19, s17, 31
	s_lshl_b32 s19, s19, 21
	s_lshl_b32 s18, s18, 7
	s_add_u32 s18, s18, s19
	s_add_u32 s14, s4, s18
	s_addc_u32 s15, s5, 0
	ds_read_b32 v100, v123
	ds_read_b32 v101, v123 offset:512
	ds_read_b32 v102, v123 offset:1024
	ds_read_b32 v103, v123 offset:1536
	ds_read_b32 v104, v123 offset:2048
	ds_read_b32 v105, v123 offset:2560
	ds_read_b32 v106, v123 offset:3072
	ds_read_b32 v107, v123 offset:3584
	ds_read_b32 v108, v123 offset:4096
	ds_read_b32 v109, v123 offset:4608
	ds_read_b32 v110, v123 offset:5120
	ds_read_b32 v111, v123 offset:5632
	ds_read_b32 v112, v123 offset:6144
	ds_read_b32 v113, v123 offset:6656
	ds_read_b32 v114, v123 offset:7168
	ds_read_b32 v115, v123 offset:7680
	s_waitcnt lgkmcnt(0)
	v_max_f32_e32 v100, v100, v100
	v_max_f32_e32 v101, v101, v101
	v_max_f32_e32 v102, v102, v102
	v_max_f32_e32 v103, v103, v103
	v_max_f32_e32 v104, v104, v104
	v_max_f32_e32 v105, v105, v105
	v_max_f32_e32 v106, v106, v106
	v_max_f32_e32 v107, v107, v107
	v_max_f32_e32 v108, v108, v108
	v_max_f32_e32 v109, v109, v109
	v_max_f32_e32 v110, v110, v110
	v_max_f32_e32 v111, v111, v111
	v_max_f32_e32 v112, v112, v112
	v_max_f32_e32 v113, v113, v113
	v_max_f32_e32 v114, v114, v114
	v_max_f32_e32 v115, v115, v115
	v_med3_f32 v100, v100, s20, v129
	v_med3_f32 v101, v101, s20, v129
	v_med3_f32 v102, v102, s20, v129
	v_med3_f32 v103, v103, s20, v129
	v_med3_f32 v104, v104, s20, v129
	v_med3_f32 v105, v105, s20, v129
	v_med3_f32 v106, v106, s20, v129
	v_med3_f32 v107, v107, s20, v129
	v_med3_f32 v108, v108, s20, v129
	v_med3_f32 v109, v109, s20, v129
	v_med3_f32 v110, v110, s20, v129
	v_med3_f32 v111, v111, s20, v129
	v_med3_f32 v112, v112, s20, v129
	v_med3_f32 v113, v113, s20, v129
	v_med3_f32 v114, v114, s20, v129
	v_med3_f32 v115, v115, s20, v129
	v_mov_b32_e32 v116, 0
	v_mov_b32_e32 v117, 0
	v_mov_b32_e32 v118, 0
	v_mov_b32_e32 v119, 0
	v_cvt_pk_fp8_f32 v116, v100, v101
	v_cvt_pk_fp8_f32 v117, v104, v105
	v_cvt_pk_fp8_f32 v118, v108, v109
	v_cvt_pk_fp8_f32 v119, v112, v113
	v_cvt_pk_fp8_f32 v116, v102, v103 op_sel:[0,0,1]
	v_cvt_pk_fp8_f32 v117, v106, v107 op_sel:[0,0,1]
	v_cvt_pk_fp8_f32 v118, v110, v111 op_sel:[0,0,1]
	v_cvt_pk_fp8_f32 v119, v114, v115 op_sel:[0,0,1]
	s_nop 0
	global_store_dwordx4 v127, v[116:119], s[14:15]
	ds_read_b32 v100, v125
	ds_read_b32 v101, v125 offset:512
	ds_read_b32 v102, v125 offset:1024
	ds_read_b32 v103, v125 offset:1536
	ds_read_b32 v104, v125 offset:2048
	ds_read_b32 v105, v125 offset:2560
	ds_read_b32 v106, v125 offset:3072
	ds_read_b32 v107, v125 offset:3584
	ds_read_b32 v108, v125 offset:4096
	ds_read_b32 v109, v125 offset:4608
	ds_read_b32 v110, v125 offset:5120
	ds_read_b32 v111, v125 offset:5632
	ds_read_b32 v112, v125 offset:6144
	ds_read_b32 v113, v125 offset:6656
	ds_read_b32 v114, v125 offset:7168
	ds_read_b32 v115, v125 offset:7680
	s_waitcnt lgkmcnt(0)
	v_max_f32_e32 v100, v100, v100
	v_max_f32_e32 v101, v101, v101
	v_max_f32_e32 v102, v102, v102
	v_max_f32_e32 v103, v103, v103
	v_max_f32_e32 v104, v104, v104
	v_max_f32_e32 v105, v105, v105
	v_max_f32_e32 v106, v106, v106
	v_max_f32_e32 v107, v107, v107
	v_max_f32_e32 v108, v108, v108
	v_max_f32_e32 v109, v109, v109
	v_max_f32_e32 v110, v110, v110
	v_max_f32_e32 v111, v111, v111
	v_max_f32_e32 v112, v112, v112
	v_max_f32_e32 v113, v113, v113
	v_max_f32_e32 v114, v114, v114
	v_max_f32_e32 v115, v115, v115
	v_med3_f32 v100, v100, s20, v129
	v_med3_f32 v101, v101, s20, v129
	v_med3_f32 v102, v102, s20, v129
	v_med3_f32 v103, v103, s20, v129
	v_med3_f32 v104, v104, s20, v129
	v_med3_f32 v105, v105, s20, v129
	v_med3_f32 v106, v106, s20, v129
	v_med3_f32 v107, v107, s20, v129
	v_med3_f32 v108, v108, s20, v129
	v_med3_f32 v109, v109, s20, v129
	v_med3_f32 v110, v110, s20, v129
	v_med3_f32 v111, v111, s20, v129
	v_med3_f32 v112, v112, s20, v129
	v_med3_f32 v113, v113, s20, v129
	v_med3_f32 v114, v114, s20, v129
	v_med3_f32 v115, v115, s20, v129
	v_mov_b32_e32 v116, 0
	v_mov_b32_e32 v117, 0
	v_mov_b32_e32 v118, 0
	v_mov_b32_e32 v119, 0
	v_cvt_pk_fp8_f32 v116, v100, v101
	v_cvt_pk_fp8_f32 v117, v104, v105
	v_cvt_pk_fp8_f32 v118, v108, v109
	v_cvt_pk_fp8_f32 v119, v112, v113
	v_cvt_pk_fp8_f32 v116, v102, v103 op_sel:[0,0,1]
	v_cvt_pk_fp8_f32 v117, v106, v107 op_sel:[0,0,1]
	v_cvt_pk_fp8_f32 v118, v110, v111 op_sel:[0,0,1]
	v_cvt_pk_fp8_f32 v119, v114, v115 op_sel:[0,0,1]
	s_nop 0
	global_store_dwordx4 v128, v[116:119], s[14:15]
	s_waitcnt vmcnt(12)
	v_mul_f32_e32 v36, 0x43000000, v36
	v_mul_f32_e32 v37, 0x43000000, v37
	v_mul_f32_e32 v38, 0x43000000, v38
	v_mul_f32_e32 v39, 0x43000000, v39
	ds_write_b128 v120, v[36:39]
	v_mul_f32_e32 v40, 0x43000000, v40
	v_mul_f32_e32 v41, 0x43000000, v41
	v_mul_f32_e32 v42, 0x43000000, v42
	v_mul_f32_e32 v43, 0x43000000, v43
	ds_write_b128 v120, v[40:43] offset:1024
	v_mul_f32_e32 v44, 0x43000000, v44
	v_mul_f32_e32 v45, 0x43000000, v45
	v_mul_f32_e32 v46, 0x43000000, v46
	v_mul_f32_e32 v47, 0x43000000, v47
	ds_write_b128 v120, v[44:47] offset:2048
	v_mul_f32_e32 v48, 0x43000000, v48
	v_mul_f32_e32 v49, 0x43000000, v49
	v_mul_f32_e32 v50, 0x43000000, v50
	v_mul_f32_e32 v51, 0x43000000, v51
	ds_write_b128 v120, v[48:51] offset:3072
	v_mul_f32_e32 v52, 0x43000000, v52
	v_mul_f32_e32 v53, 0x43000000, v53
	v_mul_f32_e32 v54, 0x43000000, v54
	v_mul_f32_e32 v55, 0x43000000, v55
	ds_write_b128 v120, v[52:55] offset:4096
	v_mul_f32_e32 v56, 0x43000000, v56
	v_mul_f32_e32 v57, 0x43000000, v57
	v_mul_f32_e32 v58, 0x43000000, v58
	v_mul_f32_e32 v59, 0x43000000, v59
	ds_write_b128 v120, v[56:59] offset:5120
	v_mul_f32_e32 v60, 0x43000000, v60
	v_mul_f32_e32 v61, 0x43000000, v61
	v_mul_f32_e32 v62, 0x43000000, v62
	v_mul_f32_e32 v63, 0x43000000, v63
	ds_write_b128 v120, v[60:63] offset:6144
	v_mul_f32_e32 v64, 0x43000000, v64
	v_mul_f32_e32 v65, 0x43000000, v65
	v_mul_f32_e32 v66, 0x43000000, v66
	v_mul_f32_e32 v67, 0x43000000, v67
	ds_write_b128 v120, v[64:67] offset:7168
	s_waitcnt lgkmcnt(0)
	s_barrier
; #define GAS __attribute__((address_space(1)))
; #define LAS __attribute__((address_space(3)))
; #define LDS_WAIT() asm volatile("s_waitcnt lgkmcnt(0)" ::: "memory")
; __device__ __forceinline__ unsigned pk4_fp8(float a, float b, float c, float d) {
;     a = fminf(fmaxf(a, -448.f), 448.f); b = fminf(fmaxf(b, -448.f), 448.f); c = fminf(fmaxf(c, -448.f), 448.f); d = fminf(fmaxf(d, -448.f), 448.f);
;     int w = __builtin_amdgcn_cvt_pk_fp8_f32(a, b, 0, false); w = __builtin_amdgcn_cvt_pk_fp8_f32(c, d, w, true); return (unsigned)w; }
;     ...
;     for (int i = 0; i < 32; ++i) v[i] = sc >= 0 ? W[(size_t)(k0 + 2 * i + (lane >> 5)) * Nsrc + sc] : 0.f;
; #pragma unroll
;     for (int i = 0; i < 32; ++i) { const int k = k0 + 2 * i + (lane >> 5); float x = v[i] * wscale; if (KS) x *= (k < ksplit ? ksA[k] : ksB[k - ksplit]); scr[(2 * i + (lane >> 5)) * 33 + (lane & 31)] = x; }
;     LDS_WAIT(); asm volatile("" ::: "memory");
;     const int c = lane & 7;
; #pragma unroll
;     for (int j = 0; j < 4; ++j) { const int n = (lane >> 3) + 8 * j; const LAS float* s = scr + (8 * c) * 33 + n;
;         const unsigned long long o = (unsigned long long)pg8::pk4_fp8(s[0 * 33], s[1 * 33], s[2 * 33], s[3 * 33]) | ((unsigned long long)pg8::pk4_fp8(s[4 * 33], s[5 * 33], s[6 * 33], s[7 * 33]) << 32);
;         *(GAS unsigned long long*)(WT + (size_t)(n0 + n) * K + k0 + 8 * c) = o; }
	s_add_i32 s17, s16, 960
	s_min_u32 s17, s17, 0x3ff
	s_lshr_b32 s18, s17, 5
	s_add_i32 s18, s18, 32
	s_and_b32 s19, s17, 31
	s_lshl_b32 s18, s18, 21
	s_lshl_b32 s19, s19, 9
	s_add_u32 s18, s18, s19
	s_add_u32 s10, s2, s18
	s_addc_u32 s11, s3, 0
	global_load_dwordx4 v[36:39], v126, s[10:11]
	s_add_u32 s10, s10, 0x8000
	s_addc_u32 s11, s11, 0
	global_load_dwordx4 v[40:43], v126, s[10:11]
	s_add_u32 s10, s10, 0x8000
	s_addc_u32 s11, s11, 0
	global_load_dwordx4 v[44:47], v126, s[10:11]
	s_add_u32 s10, s10, 0x8000
	s_addc_u32 s11, s11, 0
	global_load_dwordx4 v[48:51], v126, s[10:11]
	s_add_u32 s10, s10, 0x8000
	s_addc_u32 s11, s11, 0
	global_load_dwordx4 v[52:55], v126, s[10:11]
	s_add_u32 s10, s10, 0x8000
	s_addc_u32 s11, s11, 0
	global_load_dwordx4 v[56:59], v126, s[10:11]
	s_add_u32 s10, s10, 0x8000
	s_addc_u32 s11, s11, 0
	global_load_dwordx4 v[60:63], v126, s[10:11]
	s_add_u32 s10, s10, 0x8000
	s_addc_u32 s11, s11, 0
	global_load_dwordx4 v[64:67], v126, s[10:11]
	s_add_i32 s17, s16, 768
	s_min_u32 s17, s17, 0x3ff
	s_lshr_b32 s18, s17, 5
	s_add_i32 s18, s18, 32
	s_and_b32 s19, s17, 31
	s_lshl_b32 s19, s19, 21
	s_lshl_b32 s18, s18, 7
	s_add_u32 s18, s18, s19
	s_add_u32 s14, s4, s18
	s_addc_u32 s15, s5, 0
	ds_read_b32 v100, v122
	ds_read_b32 v101, v122 offset:512
	ds_read_b32 v102, v122 offset:1024
	ds_read_b32 v103, v122 offset:1536
	ds_read_b32 v104, v122 offset:2048
	ds_read_b32 v105, v122 offset:2560
	ds_read_b32 v106, v122 offset:3072
	ds_read_b32 v107, v122 offset:3584
	ds_read_b32 v108, v122 offset:4096
	ds_read_b32 v109, v122 offset:4608
	ds_read_b32 v110, v122 offset:5120
	ds_read_b32 v111, v122 offset:5632
	ds_read_b32 v112, v122 offset:6144
	ds_read_b32 v113, v122 offset:6656
	ds_read_b32 v114, v122 offset:7168
	ds_read_b32 v115, v122 offset:7680
	s_waitcnt lgkmcnt(0)
	v_max_f32_e32 v100, v100, v100
	v_max_f32_e32 v101, v101, v101
	v_max_f32_e32 v102, v102, v102
	v_max_f32_e32 v103, v103, v103
	v_max_f32_e32 v104, v104, v104
	v_max_f32_e32 v105, v105, v105
	v_max_f32_e32 v106, v106, v106
	v_max_f32_e32 v107, v107, v107
	v_max_f32_e32 v108, v108, v108
	v_max_f32_e32 v109, v109, v109
	v_max_f32_e32 v110, v110, v110
	v_max_f32_e32 v111, v111, v111
	v_max_f32_e32 v112, v112, v112
	v_max_f32_e32 v113, v113, v113
	v_max_f32_e32 v114, v114, v114
	v_max_f32_e32 v115, v115, v115
	v_med3_f32 v100, v100, s20, v129
	v_med3_f32 v101, v101, s20, v129
	v_med3_f32 v102, v102, s20, v129
	v_med3_f32 v103, v103, s20, v129
	v_med3_f32 v104, v104, s20, v129
	v_med3_f32 v105, v105, s20, v129
	v_med3_f32 v106, v106, s20, v129
	v_med3_f32 v107, v107, s20, v129
	v_med3_f32 v108, v108, s20, v129
	v_med3_f32 v109, v109, s20, v129
	v_med3_f32 v110, v110, s20, v129
	v_med3_f32 v111, v111, s20, v129
	v_med3_f32 v112, v112, s20, v129
	v_med3_f32 v113, v113, s20, v129
	v_med3_f32 v114, v114, s20, v129
	v_med3_f32 v115, v115, s20, v129
	v_mov_b32_e32 v116, 0
	v_mov_b32_e32 v117, 0
	v_mov_b32_e32 v118, 0
	v_mov_b32_e32 v119, 0
	v_cvt_pk_fp8_f32 v116, v100, v101
	v_cvt_pk_fp8_f32 v117, v104, v105
	v_cvt_pk_fp8_f32 v118, v108, v109
	v_cvt_pk_fp8_f32 v119, v112, v113
	v_cvt_pk_fp8_f32 v116, v102, v103 op_sel:[0,0,1]
	v_cvt_pk_fp8_f32 v117, v106, v107 op_sel:[0,0,1]
	v_cvt_pk_fp8_f32 v118, v110, v111 op_sel:[0,0,1]
	v_cvt_pk_fp8_f32 v119, v114, v115 op_sel:[0,0,1]
	s_nop 0
	global_store_dwordx4 v127, v[116:119], s[14:15]
	ds_read_b32 v100, v124
	ds_read_b32 v101, v124 offset:512
	ds_read_b32 v102, v124 offset:1024
	ds_read_b32 v103, v124 offset:1536
	ds_read_b32 v104, v124 offset:2048
	ds_read_b32 v105, v124 offset:2560
	ds_read_b32 v106, v124 offset:3072
	ds_read_b32 v107, v124 offset:3584
	ds_read_b32 v108, v124 offset:4096
	ds_read_b32 v109, v124 offset:4608
	ds_read_b32 v110, v124 offset:5120
	ds_read_b32 v111, v124 offset:5632
	ds_read_b32 v112, v124 offset:6144
	ds_read_b32 v113, v124 offset:6656
	ds_read_b32 v114, v124 offset:7168
	ds_read_b32 v115, v124 offset:7680
	s_waitcnt lgkmcnt(0)
	v_max_f32_e32 v100, v100, v100
	v_max_f32_e32 v101, v101, v101
	v_max_f32_e32 v102, v102, v102
	v_max_f32_e32 v103, v103, v103
	v_max_f32_e32 v104, v104, v104
	v_max_f32_e32 v105, v105, v105
	v_max_f32_e32 v106, v106, v106
	v_max_f32_e32 v107, v107, v107
	v_max_f32_e32 v108, v108, v108
	v_max_f32_e32 v109, v109, v109
	v_max_f32_e32 v110, v110, v110
	v_max_f32_e32 v111, v111, v111
	v_max_f32_e32 v112, v112, v112
	v_max_f32_e32 v113, v113, v113
	v_max_f32_e32 v114, v114, v114
	v_max_f32_e32 v115, v115, v115
	v_med3_f32 v100, v100, s20, v129
	v_med3_f32 v101, v101, s20, v129
	v_med3_f32 v102, v102, s20, v129
	v_med3_f32 v103, v103, s20, v129
	v_med3_f32 v104, v104, s20, v129
	v_med3_f32 v105, v105, s20, v129
	v_med3_f32 v106, v106, s20, v129
	v_med3_f32 v107, v107, s20, v129
	v_med3_f32 v108, v108, s20, v129
	v_med3_f32 v109, v109, s20, v129
	v_med3_f32 v110, v110, s20, v129
	v_med3_f32 v111, v111, s20, v129
	v_med3_f32 v112, v112, s20, v129
	v_med3_f32 v113, v113, s20, v129
	v_med3_f32 v114, v114, s20, v129
	v_med3_f32 v115, v115, s20, v129
	v_mov_b32_e32 v116, 0
	v_mov_b32_e32 v117, 0
	v_mov_b32_e32 v118, 0
	v_mov_b32_e32 v119, 0
	v_cvt_pk_fp8_f32 v116, v100, v101
	v_cvt_pk_fp8_f32 v117, v104, v105
	v_cvt_pk_fp8_f32 v118, v108, v109
	v_cvt_pk_fp8_f32 v119, v112, v113
	v_cvt_pk_fp8_f32 v116, v102, v103 op_sel:[0,0,1]
	v_cvt_pk_fp8_f32 v117, v106, v107 op_sel:[0,0,1]
	v_cvt_pk_fp8_f32 v118, v110, v111 op_sel:[0,0,1]
	v_cvt_pk_fp8_f32 v119, v114, v115 op_sel:[0,0,1]
	s_nop 0
	global_store_dwordx4 v128, v[116:119], s[14:15]
	s_waitcnt vmcnt(12)
	v_mul_f32_e32 v68, 0x43000000, v68
	v_mul_f32_e32 v69, 0x43000000, v69
	v_mul_f32_e32 v70, 0x43000000, v70
	v_mul_f32_e32 v71, 0x43000000, v71
	ds_write_b128 v121, v[68:71]
	v_mul_f32_e32 v72, 0x43000000, v72
	v_mul_f32_e32 v73, 0x43000000, v73
	v_mul_f32_e32 v74, 0x43000000, v74
	v_mul_f32_e32 v75, 0x43000000, v75
	ds_write_b128 v121, v[72:75] offset:1024
	v_mul_f32_e32 v76, 0x43000000, v76
	v_mul_f32_e32 v77, 0x43000000, v77
	v_mul_f32_e32 v78, 0x43000000, v78
	v_mul_f32_e32 v79, 0x43000000, v79
	ds_write_b128 v121, v[76:79] offset:2048
	v_mul_f32_e32 v80, 0x43000000, v80
	v_mul_f32_e32 v81, 0x43000000, v81
	v_mul_f32_e32 v82, 0x43000000, v82
	v_mul_f32_e32 v83, 0x43000000, v83
	ds_write_b128 v121, v[80:83] offset:3072
	v_mul_f32_e32 v84, 0x43000000, v84
	v_mul_f32_e32 v85, 0x43000000, v85
	v_mul_f32_e32 v86, 0x43000000, v86
	v_mul_f32_e32 v87, 0x43000000, v87
	ds_write_b128 v121, v[84:87] offset:4096
	v_mul_f32_e32 v88, 0x43000000, v88
	v_mul_f32_e32 v89, 0x43000000, v89
	v_mul_f32_e32 v90, 0x43000000, v90
	v_mul_f32_e32 v91, 0x43000000, v91
	ds_write_b128 v121, v[88:91] offset:5120
	v_mul_f32_e32 v92, 0x43000000, v92
	v_mul_f32_e32 v93, 0x43000000, v93
	v_mul_f32_e32 v94, 0x43000000, v94
	v_mul_f32_e32 v95, 0x43000000, v95
	ds_write_b128 v121, v[92:95] offset:6144
	v_mul_f32_e32 v96, 0x43000000, v96
	v_mul_f32_e32 v97, 0x43000000, v97
	v_mul_f32_e32 v98, 0x43000000, v98
	v_mul_f32_e32 v99, 0x43000000, v99
	ds_write_b128 v121, v[96:99] offset:7168
	s_waitcnt lgkmcnt(0)
	s_barrier
; #define GAS __attribute__((address_space(1)))
; #define LAS __attribute__((address_space(3)))
; #define LDS_WAIT() asm volatile("s_waitcnt lgkmcnt(0)" ::: "memory")
; __device__ __forceinline__ unsigned pk4_fp8(float a, float b, float c, float d) {
;     a = fminf(fmaxf(a, -448.f), 448.f); b = fminf(fmaxf(b, -448.f), 448.f); c = fminf(fmaxf(c, -448.f), 448.f); d = fminf(fmaxf(d, -448.f), 448.f);
;     int w = __builtin_amdgcn_cvt_pk_fp8_f32(a, b, 0, false); w = __builtin_amdgcn_cvt_pk_fp8_f32(c, d, w, true); return (unsigned)w; }
;     ...
;     for (int i = 0; i < 32; ++i) v[i] = sc >= 0 ? W[(size_t)(k0 + 2 * i + (lane >> 5)) * Nsrc + sc] : 0.f;
; #pragma unroll
;     for (int i = 0; i < 32; ++i) { const int k = k0 + 2 * i + (lane >> 5); float x = v[i] * wscale; if (KS) x *= (k < ksplit ? ksA[k] : ksB[k - ksplit]); scr[(2 * i + (lane >> 5)) * 33 + (lane & 31)] = x; }
;     LDS_WAIT(); asm volatile("" ::: "memory");
;     const int c = lane & 7;
; #pragma unroll
;     for (int j = 0; j < 4; ++j) { const int n = (lane >> 3) + 8 * j; const LAS float* s = scr + (8 * c) * 33 + n;
;         const unsigned long long o = (unsigned long long)pg8::pk4_fp8(s[0 * 33], s[1 * 33], s[2 * 33], s[3 * 33]) | ((unsigned long long)pg8::pk4_fp8(s[4 * 33], s[5 * 33], s[6 * 33], s[7 * 33]) << 32);
;         *(GAS unsigned long long*)(WT + (size_t)(n0 + n) * K + k0 + 8 * c) = o; }
	s_add_i32 s17, s16, 864
	s_min_u32 s17, s17, 0x3ff
	s_lshr_b32 s18, s17, 5
	s_add_i32 s18, s18, 32
	s_and_b32 s19, s17, 31
	s_lshl_b32 s19, s19, 21
	s_lshl_b32 s18, s18, 7
	s_add_u32 s18, s18, s19
	s_add_u32 s14, s4, s18
	s_addc_u32 s15, s5, 0
	ds_read_b32 v100, v123
	ds_read_b32 v101, v123 offset:512
	ds_read_b32 v102, v123 offset:1024
	ds_read_b32 v103, v123 offset:1536
	ds_read_b32 v104, v123 offset:2048
	ds_read_b32 v105, v123 offset:2560
	ds_read_b32 v106, v123 offset:3072
	ds_read_b32 v107, v123 offset:3584
	ds_read_b32 v108, v123 offset:4096
	ds_read_b32 v109, v123 offset:4608
	ds_read_b32 v110, v123 offset:5120
	ds_read_b32 v111, v123 offset:5632
	ds_read_b32 v112, v123 offset:6144
	ds_read_b32 v113, v123 offset:6656
	ds_read_b32 v114, v123 offset:7168
	ds_read_b32 v115, v123 offset:7680
	s_waitcnt lgkmcnt(0)
	v_max_f32_e32 v100, v100, v100
	v_max_f32_e32 v101, v101, v101
	v_max_f32_e32 v102, v102, v102
	v_max_f32_e32 v103, v103, v103
	v_max_f32_e32 v104, v104, v104
	v_max_f32_e32 v105, v105, v105
	v_max_f32_e32 v106, v106, v106
	v_max_f32_e32 v107, v107, v107
	v_max_f32_e32 v108, v108, v108
	v_max_f32_e32 v109, v109, v109
	v_max_f32_e32 v110, v110, v110
	v_max_f32_e32 v111, v111, v111
	v_max_f32_e32 v112, v112, v112
	v_max_f32_e32 v113, v113, v113
	v_max_f32_e32 v114, v114, v114
	v_max_f32_e32 v115, v115, v115
	v_med3_f32 v100, v100, s20, v129
	v_med3_f32 v101, v101, s20, v129
	v_med3_f32 v102, v102, s20, v129
	v_med3_f32 v103, v103, s20, v129
	v_med3_f32 v104, v104, s20, v129
	v_med3_f32 v105, v105, s20, v129
	v_med3_f32 v106, v106, s20, v129
	v_med3_f32 v107, v107, s20, v129
	v_med3_f32 v108, v108, s20, v129
	v_med3_f32 v109, v109, s20, v129
	v_med3_f32 v110, v110, s20, v129
	v_med3_f32 v111, v111, s20, v129
	v_med3_f32 v112, v112, s20, v129
	v_med3_f32 v113, v113, s20, v129
	v_med3_f32 v114, v114, s20, v129
	v_med3_f32 v115, v115, s20, v129
	v_mov_b32_e32 v116, 0
	v_mov_b32_e32 v117, 0
	v_mov_b32_e32 v118, 0
	v_mov_b32_e32 v119, 0
	v_cvt_pk_fp8_f32 v116, v100, v101
	v_cvt_pk_fp8_f32 v117, v104, v105
	v_cvt_pk_fp8_f32 v118, v108, v109
	v_cvt_pk_fp8_f32 v119, v112, v113
	v_cvt_pk_fp8_f32 v116, v102, v103 op_sel:[0,0,1]
	v_cvt_pk_fp8_f32 v117, v106, v107 op_sel:[0,0,1]
	v_cvt_pk_fp8_f32 v118, v110, v111 op_sel:[0,0,1]
	v_cvt_pk_fp8_f32 v119, v114, v115 op_sel:[0,0,1]
	s_nop 0
	global_store_dwordx4 v127, v[116:119], s[14:15]
	ds_read_b32 v100, v125
	ds_read_b32 v101, v125 offset:512
	ds_read_b32 v102, v125 offset:1024
	ds_read_b32 v103, v125 offset:1536
	ds_read_b32 v104, v125 offset:2048
	ds_read_b32 v105, v125 offset:2560
	ds_read_b32 v106, v125 offset:3072
	ds_read_b32 v107, v125 offset:3584
	ds_read_b32 v108, v125 offset:4096
	ds_read_b32 v109, v125 offset:4608
	ds_read_b32 v110, v125 offset:5120
	ds_read_b32 v111, v125 offset:5632
	ds_read_b32 v112, v125 offset:6144
	ds_read_b32 v113, v125 offset:6656
	ds_read_b32 v114, v125 offset:7168
	ds_read_b32 v115, v125 offset:7680
	s_waitcnt lgkmcnt(0)
	v_max_f32_e32 v100, v100, v100
	v_max_f32_e32 v101, v101, v101
	v_max_f32_e32 v102, v102, v102
	v_max_f32_e32 v103, v103, v103
	v_max_f32_e32 v104, v104, v104
	v_max_f32_e32 v105, v105, v105
	v_max_f32_e32 v106, v106, v106
	v_max_f32_e32 v107, v107, v107
	v_max_f32_e32 v108, v108, v108
	v_max_f32_e32 v109, v109, v109
	v_max_f32_e32 v110, v110, v110
	v_max_f32_e32 v111, v111, v111
	v_max_f32_e32 v112, v112, v112
	v_max_f32_e32 v113, v113, v113
	v_max_f32_e32 v114, v114, v114
	v_max_f32_e32 v115, v115, v115
	v_med3_f32 v100, v100, s20, v129
	v_med3_f32 v101, v101, s20, v129
	v_med3_f32 v102, v102, s20, v129
	v_med3_f32 v103, v103, s20, v129
	v_med3_f32 v104, v104, s20, v129
	v_med3_f32 v105, v105, s20, v129
	v_med3_f32 v106, v106, s20, v129
	v_med3_f32 v107, v107, s20, v129
	v_med3_f32 v108, v108, s20, v129
	v_med3_f32 v109, v109, s20, v129
	v_med3_f32 v110, v110, s20, v129
	v_med3_f32 v111, v111, s20, v129
	v_med3_f32 v112, v112, s20, v129
	v_med3_f32 v113, v113, s20, v129
	v_med3_f32 v114, v114, s20, v129
	v_med3_f32 v115, v115, s20, v129
	v_mov_b32_e32 v116, 0
	v_mov_b32_e32 v117, 0
	v_mov_b32_e32 v118, 0
	v_mov_b32_e32 v119, 0
	v_cvt_pk_fp8_f32 v116, v100, v101
	v_cvt_pk_fp8_f32 v117, v104, v105
	v_cvt_pk_fp8_f32 v118, v108, v109
	v_cvt_pk_fp8_f32 v119, v112, v113
	v_cvt_pk_fp8_f32 v116, v102, v103 op_sel:[0,0,1]
	v_cvt_pk_fp8_f32 v117, v106, v107 op_sel:[0,0,1]
	v_cvt_pk_fp8_f32 v118, v110, v111 op_sel:[0,0,1]
	v_cvt_pk_fp8_f32 v119, v114, v115 op_sel:[0,0,1]
	s_nop 0
	global_store_dwordx4 v128, v[116:119], s[14:15]
	s_waitcnt vmcnt(4)
	v_mul_f32_e32 v36, 0x43000000, v36
	v_mul_f32_e32 v37, 0x43000000, v37
	v_mul_f32_e32 v38, 0x43000000, v38
	v_mul_f32_e32 v39, 0x43000000, v39
	ds_write_b128 v120, v[36:39]
	v_mul_f32_e32 v40, 0x43000000, v40
	v_mul_f32_e32 v41, 0x43000000, v41
	v_mul_f32_e32 v42, 0x43000000, v42
	v_mul_f32_e32 v43, 0x43000000, v43
	ds_write_b128 v120, v[40:43] offset:1024
	v_mul_f32_e32 v44, 0x43000000, v44
	v_mul_f32_e32 v45, 0x43000000, v45
	v_mul_f32_e32 v46, 0x43000000, v46
	v_mul_f32_e32 v47, 0x43000000, v47
	ds_write_b128 v120, v[44:47] offset:2048
	v_mul_f32_e32 v48, 0x43000000, v48
	v_mul_f32_e32 v49, 0x43000000, v49
	v_mul_f32_e32 v50, 0x43000000, v50
	v_mul_f32_e32 v51, 0x43000000, v51
	ds_write_b128 v120, v[48:51] offset:3072
	v_mul_f32_e32 v52, 0x43000000, v52
	v_mul_f32_e32 v53, 0x43000000, v53
	v_mul_f32_e32 v54, 0x43000000, v54
	v_mul_f32_e32 v55, 0x43000000, v55
	ds_write_b128 v120, v[52:55] offset:4096
	v_mul_f32_e32 v56, 0x43000000, v56
	v_mul_f32_e32 v57, 0x43000000, v57
	v_mul_f32_e32 v58, 0x43000000, v58
	v_mul_f32_e32 v59, 0x43000000, v59
	ds_write_b128 v120, v[56:59] offset:5120
	v_mul_f32_e32 v60, 0x43000000, v60
	v_mul_f32_e32 v61, 0x43000000, v61
	v_mul_f32_e32 v62, 0x43000000, v62
	v_mul_f32_e32 v63, 0x43000000, v63
	ds_write_b128 v120, v[60:63] offset:6144
	v_mul_f32_e32 v64, 0x43000000, v64
	v_mul_f32_e32 v65, 0x43000000, v65
	v_mul_f32_e32 v66, 0x43000000, v66
	v_mul_f32_e32 v67, 0x43000000, v67
	ds_write_b128 v120, v[64:67] offset:7168
	s_waitcnt lgkmcnt(0)
	s_barrier
; #define GAS __attribute__((address_space(1)))
; #define LAS __attribute__((address_space(3)))
; #define LDS_WAIT() asm volatile("s_waitcnt lgkmcnt(0)" ::: "memory")
; __device__ __forceinline__ unsigned pk4_fp8(float a, float b, float c, float d) {
;     a = fminf(fmaxf(a, -448.f), 448.f); b = fminf(fmaxf(b, -448.f), 448.f); c = fminf(fmaxf(c, -448.f), 448.f); d = fminf(fmaxf(d, -448.f), 448.f);
;     int w = __builtin_amdgcn_cvt_pk_fp8_f32(a, b, 0, false); w = __builtin_amdgcn_cvt_pk_fp8_f32(c, d, w, true); return (unsigned)w; }
;     ...
;     for (int i = 0; i < 32; ++i) v[i] = sc >= 0 ? W[(size_t)(k0 + 2 * i + (lane >> 5)) * Nsrc + sc] : 0.f;
; #pragma unroll
;     for (int i = 0; i < 32; ++i) { const int k = k0 + 2 * i + (lane >> 5); float x = v[i] * wscale; if (KS) x *= (k < ksplit ? ksA[k] : ksB[k - ksplit]); scr[(2 * i + (lane >> 5)) * 33 + (lane & 31)] = x; }
;     LDS_WAIT(); asm volatile("" ::: "memory");
;     const int c = lane & 7;
; #pragma unroll
;     for (int j = 0; j < 4; ++j) { const int n = (lane >> 3) + 8 * j; const LAS float* s = scr + (8 * c) * 33 + n;
;         const unsigned long long o = (unsigned long long)pg8::pk4_fp8(s[0 * 33], s[1 * 33], s[2 * 33], s[3 * 33]) | ((unsigned long long)pg8::pk4_fp8(s[4 * 33], s[5 * 33], s[6 * 33], s[7 * 33]) << 32);
;         *(GAS unsigned long long*)(WT + (size_t)(n0 + n) * K + k0 + 8 * c) = o; }
	s_add_i32 s17, s16, 960
	s_min_u32 s17, s17, 0x3ff
	s_lshr_b32 s18, s17, 5
	s_add_i32 s18, s18, 32
	s_and_b32 s19, s17, 31
	s_lshl_b32 s19, s19, 21
	s_lshl_b32 s18, s18, 7
	s_add_u32 s18, s18, s19
	s_add_u32 s14, s4, s18
	s_addc_u32 s15, s5, 0
	ds_read_b32 v100, v122
	ds_read_b32 v101, v122 offset:512
	ds_read_b32 v102, v122 offset:1024
	ds_read_b32 v103, v122 offset:1536
	ds_read_b32 v104, v122 offset:2048
	ds_read_b32 v105, v122 offset:2560
	ds_read_b32 v106, v122 offset:3072
	ds_read_b32 v107, v122 offset:3584
	ds_read_b32 v108, v122 offset:4096
	ds_read_b32 v109, v122 offset:4608
	ds_read_b32 v110, v122 offset:5120
	ds_read_b32 v111, v122 offset:5632
	ds_read_b32 v112, v122 offset:6144
	ds_read_b32 v113, v122 offset:6656
	ds_read_b32 v114, v122 offset:7168
	ds_read_b32 v115, v122 offset:7680
	s_waitcnt lgkmcnt(0)
	v_max_f32_e32 v100, v100, v100
	v_max_f32_e32 v101, v101, v101
	v_max_f32_e32 v102, v102, v102
	v_max_f32_e32 v103, v103, v103
	v_max_f32_e32 v104, v104, v104
	v_max_f32_e32 v105, v105, v105
	v_max_f32_e32 v106, v106, v106
	v_max_f32_e32 v107, v107, v107
	v_max_f32_e32 v108, v108, v108
	v_max_f32_e32 v109, v109, v109
	v_max_f32_e32 v110, v110, v110
	v_max_f32_e32 v111, v111, v111
	v_max_f32_e32 v112, v112, v112
	v_max_f32_e32 v113, v113, v113
	v_max_f32_e32 v114, v114, v114
	v_max_f32_e32 v115, v115, v115
	v_med3_f32 v100, v100, s20, v129
	v_med3_f32 v101, v101, s20, v129
	v_med3_f32 v102, v102, s20, v129
	v_med3_f32 v103, v103, s20, v129
	v_med3_f32 v104, v104, s20, v129
	v_med3_f32 v105, v105, s20, v129
	v_med3_f32 v106, v106, s20, v129
	v_med3_f32 v107, v107, s20, v129
	v_med3_f32 v108, v108, s20, v129
	v_med3_f32 v109, v109, s20, v129
	v_med3_f32 v110, v110, s20, v129
	v_med3_f32 v111, v111, s20, v129
	v_med3_f32 v112, v112, s20, v129
	v_med3_f32 v113, v113, s20, v129
	v_med3_f32 v114, v114, s20, v129
	v_med3_f32 v115, v115, s20, v129
	v_mov_b32_e32 v116, 0
	v_mov_b32_e32 v117, 0
	v_mov_b32_e32 v118, 0
	v_mov_b32_e32 v119, 0
	v_cvt_pk_fp8_f32 v116, v100, v101
	v_cvt_pk_fp8_f32 v117, v104, v105
	v_cvt_pk_fp8_f32 v118, v108, v109
	v_cvt_pk_fp8_f32 v119, v112, v113
	v_cvt_pk_fp8_f32 v116, v102, v103 op_sel:[0,0,1]
	v_cvt_pk_fp8_f32 v117, v106, v107 op_sel:[0,0,1]
	v_cvt_pk_fp8_f32 v118, v110, v111 op_sel:[0,0,1]
	v_cvt_pk_fp8_f32 v119, v114, v115 op_sel:[0,0,1]
	s_nop 0
	global_store_dwordx4 v127, v[116:119], s[14:15]
	ds_read_b32 v100, v124
	ds_read_b32 v101, v124 offset:512
	ds_read_b32 v102, v124 offset:1024
	ds_read_b32 v103, v124 offset:1536
	ds_read_b32 v104, v124 offset:2048
	ds_read_b32 v105, v124 offset:2560
	ds_read_b32 v106, v124 offset:3072
	ds_read_b32 v107, v124 offset:3584
	ds_read_b32 v108, v124 offset:4096
	ds_read_b32 v109, v124 offset:4608
	ds_read_b32 v110, v124 offset:5120
	ds_read_b32 v111, v124 offset:5632
	ds_read_b32 v112, v124 offset:6144
	ds_read_b32 v113, v124 offset:6656
	ds_read_b32 v114, v124 offset:7168
	ds_read_b32 v115, v124 offset:7680
	s_waitcnt lgkmcnt(0)
	v_max_f32_e32 v100, v100, v100
	v_max_f32_e32 v101, v101, v101
	v_max_f32_e32 v102, v102, v102
	v_max_f32_e32 v103, v103, v103
	v_max_f32_e32 v104, v104, v104
	v_max_f32_e32 v105, v105, v105
	v_max_f32_e32 v106, v106, v106
	v_max_f32_e32 v107, v107, v107
	v_max_f32_e32 v108, v108, v108
	v_max_f32_e32 v109, v109, v109
	v_max_f32_e32 v110, v110, v110
	v_max_f32_e32 v111, v111, v111
	v_max_f32_e32 v112, v112, v112
	v_max_f32_e32 v113, v113, v113
	v_max_f32_e32 v114, v114, v114
	v_max_f32_e32 v115, v115, v115
	v_med3_f32 v100, v100, s20, v129
	v_med3_f32 v101, v101, s20, v129
	v_med3_f32 v102, v102, s20, v129
	v_med3_f32 v103, v103, s20, v129
	v_med3_f32 v104, v104, s20, v129
	v_med3_f32 v105, v105, s20, v129
	v_med3_f32 v106, v106, s20, v129
	v_med3_f32 v107, v107, s20, v129
	v_med3_f32 v108, v108, s20, v129
	v_med3_f32 v109, v109, s20, v129
	v_med3_f32 v110, v110, s20, v129
	v_med3_f32 v111, v111, s20, v129
	v_med3_f32 v112, v112, s20, v129
	v_med3_f32 v113, v113, s20, v129
	v_med3_f32 v114, v114, s20, v129
	v_med3_f32 v115, v115, s20, v129
	v_mov_b32_e32 v116, 0
	v_mov_b32_e32 v117, 0
	v_mov_b32_e32 v118, 0
	v_mov_b32_e32 v119, 0
	v_cvt_pk_fp8_f32 v116, v100, v101
	v_cvt_pk_fp8_f32 v117, v104, v105
	v_cvt_pk_fp8_f32 v118, v108, v109
	v_cvt_pk_fp8_f32 v119, v112, v113
	v_cvt_pk_fp8_f32 v116, v102, v103 op_sel:[0,0,1]
	v_cvt_pk_fp8_f32 v117, v106, v107 op_sel:[0,0,1]
	v_cvt_pk_fp8_f32 v118, v110, v111 op_sel:[0,0,1]
	v_cvt_pk_fp8_f32 v119, v114, v115 op_sel:[0,0,1]
	s_nop 0
	global_store_dwordx4 v128, v[116:119], s[14:15]
	s_waitcnt vmcnt(0) lgkmcnt(0)
	s_barrier
